# v065 + mid-segment s_setprio 0/1 yield pairs removed from all bf16/fp8 GEMM K loops
# speedup vs baseline: 1.0062x; 1.0003x over previous
.LBB0_622:
	s_add_i32 s71, s60, 2
	s_add_u32 s7, s38, 0x80
	s_addc_u32 s10, s39, 0
	s_add_i32 s72, 0, 0x10000
	s_cmp_eq_u32 s64, s60
	s_cselect_b32 s61, s57, s10
	s_cselect_b32 s60, s56, s7
	s_cselect_b32 s11, s59, s63
	s_cselect_b32 s10, s58, s62
	s_add_i32 s7, 0, 0x14000
	v_add_u32_e32 v118, s72, v189
	v_add_u32_e32 v158, s7, v189
	ds_read_b128 v[106:109], v118
	ds_read_b128 v[110:113], v118 offset:1024
	ds_read_b128 v[114:117], v118 offset:2048
	ds_read_b128 v[118:121], v118 offset:3072
	ds_read_b128 v[146:149], v158
	ds_read_b128 v[150:153], v158 offset:1024
	ds_read_b128 v[154:157], v158 offset:2048
	ds_read_b128 v[158:161], v158 offset:3072
	v_lshl_add_u64 v[200:201], s[38:39], 0, v[168:169]
	s_add_i32 m0, s16, 0xc000
	ds_read_b128 v[172:175], v191
	ds_read_b128 v[176:179], v191 offset:1024
	ds_read_b128 v[180:183], v191 offset:2048
	ds_read_b128 v[192:195], v191 offset:3072
	ds_read_b128 v[196:199], v191 offset:4096
	ds_read_b128 v[210:213], v191 offset:5120
	ds_read_b128 v[214:217], v191 offset:6144
	ds_read_b128 v[218:221], v191 offset:7168
	global_load_lds_dwordx4 v[200:201], off
	v_lshl_add_u64 v[200:201], s[38:39], 0, v[170:171]
	s_add_i32 m0, s16, 0xe000
	s_nop 0
	global_load_lds_dwordx4 v[200:201], off
	s_waitcnt vmcnt(8)
	s_waitcnt lgkmcnt(0)
	s_setprio 1
	s_barrier
	v_mfma_f32_16x16x32_bf16 v[62:65], v[106:109], v[172:175], v[62:65]
	v_mfma_f32_16x16x32_bf16 v[58:61], v[114:117], v[172:175], v[58:61]
	v_mfma_f32_16x16x32_bf16 v[54:57], v[106:109], v[180:183], v[54:57]
	v_mfma_f32_16x16x32_bf16 v[50:53], v[114:117], v[180:183], v[50:53]
	v_mfma_f32_16x16x32_bf16 v[46:49], v[106:109], v[196:199], v[46:49]
	v_mfma_f32_16x16x32_bf16 v[42:45], v[114:117], v[196:199], v[42:45]
	v_mfma_f32_16x16x32_bf16 v[38:41], v[106:109], v[214:217], v[38:41]
	v_mfma_f32_16x16x32_bf16 v[34:37], v[114:117], v[214:217], v[34:37]
	v_mfma_f32_16x16x32_bf16 v[62:65], v[110:113], v[176:179], v[62:65]
	v_mfma_f32_16x16x32_bf16 v[58:61], v[118:121], v[176:179], v[58:61]
	v_mfma_f32_16x16x32_bf16 v[54:57], v[110:113], v[192:195], v[54:57]
	v_mfma_f32_16x16x32_bf16 v[50:53], v[118:121], v[192:195], v[50:53]
	v_mfma_f32_16x16x32_bf16 v[46:49], v[110:113], v[210:213], v[46:49]
	v_mfma_f32_16x16x32_bf16 v[42:45], v[118:121], v[210:213], v[42:45]
	v_mfma_f32_16x16x32_bf16 v[38:41], v[110:113], v[218:221], v[38:41]
	v_mfma_f32_16x16x32_bf16 v[34:37], v[118:121], v[218:221], v[34:37]
	v_mfma_f32_16x16x32_bf16 v[142:145], v[146:149], v[172:175], v[142:145]
	v_mfma_f32_16x16x32_bf16 v[138:141], v[154:157], v[172:175], v[138:141]
	v_mfma_f32_16x16x32_bf16 v[134:137], v[146:149], v[180:183], v[134:137]
	v_mfma_f32_16x16x32_bf16 v[130:133], v[154:157], v[180:183], v[130:133]
	v_mfma_f32_16x16x32_bf16 v[126:129], v[146:149], v[196:199], v[126:129]
	v_mfma_f32_16x16x32_bf16 v[122:125], v[154:157], v[196:199], v[122:125]
	v_mfma_f32_16x16x32_bf16 v[102:105], v[146:149], v[214:217], v[102:105]
	v_mfma_f32_16x16x32_bf16 v[98:101], v[154:157], v[214:217], v[98:101]
	v_mfma_f32_16x16x32_bf16 v[142:145], v[150:153], v[176:179], v[142:145]
	v_mfma_f32_16x16x32_bf16 v[138:141], v[158:161], v[176:179], v[138:141]
	v_mfma_f32_16x16x32_bf16 v[134:137], v[150:153], v[192:195], v[134:137]
	v_mfma_f32_16x16x32_bf16 v[130:133], v[158:161], v[192:195], v[130:133]
	v_mfma_f32_16x16x32_bf16 v[126:129], v[150:153], v[210:213], v[126:129]
	v_mfma_f32_16x16x32_bf16 v[122:125], v[158:161], v[210:213], v[122:125]
	v_mfma_f32_16x16x32_bf16 v[102:105], v[150:153], v[218:221], v[102:105]
	v_mfma_f32_16x16x32_bf16 v[98:101], v[158:161], v[218:221], v[98:101]
	s_setprio 0
	s_barrier
	s_add_i32 s72, s72, s13
	v_lshl_add_u64 v[200:201], s[10:11], 0, v[0:1]
	s_mov_b32 m0, s72
	ds_read_b128 v[172:175], v191 offset:16384
	ds_read_b128 v[176:179], v191 offset:17408
	ds_read_b128 v[180:183], v191 offset:18432
	ds_read_b128 v[192:195], v191 offset:19456
	ds_read_b128 v[196:199], v191 offset:20480
	ds_read_b128 v[210:213], v191 offset:21504
	ds_read_b128 v[214:217], v191 offset:22528
	ds_read_b128 v[218:221], v191 offset:23552
	global_load_lds_dwordx4 v[200:201], off
	s_add_i32 m0, s72, 0x2000
	v_lshl_add_u64 v[222:223], s[10:11], 0, v[166:167]
	s_add_u32 s10, s10, s0
	s_addc_u32 s11, s11, s1
	s_add_i32 s7, s7, s13
	global_load_lds_dwordx4 v[222:223], off
	v_lshl_add_u64 v[224:225], s[10:11], 0, v[0:1]
	s_mov_b32 m0, s7
	v_lshl_add_u64 v[226:227], s[10:11], 0, v[166:167]
	global_load_lds_dwordx4 v[224:225], off
	s_add_i32 m0, s7, 0x2000
	v_lshl_add_u64 v[228:229], s[60:61], 0, v[162:163]
	global_load_lds_dwordx4 v[226:227], off
	s_mov_b32 m0, s16
	v_lshl_add_u64 v[230:231], s[60:61], 0, v[164:165]
	global_load_lds_dwordx4 v[228:229], off
	s_mov_b32 m0, s17
	s_nop 0
	global_load_lds_dwordx4 v[230:231], off
	s_waitcnt vmcnt(8)
	s_waitcnt lgkmcnt(0)
	s_setprio 1
	s_barrier
	v_mfma_f32_16x16x32_bf16 v[30:33], v[106:109], v[172:175], v[30:33]
	v_mfma_f32_16x16x32_bf16 v[26:29], v[114:117], v[172:175], v[26:29]
	v_mfma_f32_16x16x32_bf16 v[22:25], v[106:109], v[180:183], v[22:25]
	v_mfma_f32_16x16x32_bf16 v[18:21], v[114:117], v[180:183], v[18:21]
	v_mfma_f32_16x16x32_bf16 v[14:17], v[106:109], v[196:199], v[14:17]
	v_mfma_f32_16x16x32_bf16 v[10:13], v[114:117], v[196:199], v[10:13]
	v_mfma_f32_16x16x32_bf16 v[6:9], v[106:109], v[214:217], v[6:9]
	v_mfma_f32_16x16x32_bf16 v[2:5], v[114:117], v[214:217], v[2:5]
	v_mfma_f32_16x16x32_bf16 v[30:33], v[110:113], v[176:179], v[30:33]
	v_mfma_f32_16x16x32_bf16 v[26:29], v[118:121], v[176:179], v[26:29]
	v_mfma_f32_16x16x32_bf16 v[22:25], v[110:113], v[192:195], v[22:25]
	v_mfma_f32_16x16x32_bf16 v[18:21], v[118:121], v[192:195], v[18:21]
	v_mfma_f32_16x16x32_bf16 v[14:17], v[110:113], v[210:213], v[14:17]
	v_mfma_f32_16x16x32_bf16 v[10:13], v[118:121], v[210:213], v[10:13]
	v_mfma_f32_16x16x32_bf16 v[6:9], v[110:113], v[218:221], v[6:9]
	v_mfma_f32_16x16x32_bf16 v[2:5], v[118:121], v[218:221], v[2:5]
	v_mfma_f32_16x16x32_bf16 v[94:97], v[146:149], v[172:175], v[94:97]
	v_mfma_f32_16x16x32_bf16 v[90:93], v[154:157], v[172:175], v[90:93]
	v_mfma_f32_16x16x32_bf16 v[86:89], v[146:149], v[180:183], v[86:89]
	v_mfma_f32_16x16x32_bf16 v[82:85], v[154:157], v[180:183], v[82:85]
	v_mfma_f32_16x16x32_bf16 v[78:81], v[146:149], v[196:199], v[78:81]
	v_mfma_f32_16x16x32_bf16 v[74:77], v[154:157], v[196:199], v[74:77]
	v_mfma_f32_16x16x32_bf16 v[70:73], v[146:149], v[214:217], v[70:73]
	v_mfma_f32_16x16x32_bf16 v[66:69], v[154:157], v[214:217], v[66:69]
	v_mfma_f32_16x16x32_bf16 v[94:97], v[150:153], v[176:179], v[94:97]
	v_mfma_f32_16x16x32_bf16 v[90:93], v[158:161], v[176:179], v[90:93]
	v_mfma_f32_16x16x32_bf16 v[86:89], v[150:153], v[192:195], v[86:89]
	v_mfma_f32_16x16x32_bf16 v[82:85], v[158:161], v[192:195], v[82:85]
	v_mfma_f32_16x16x32_bf16 v[78:81], v[150:153], v[210:213], v[78:81]
	v_mfma_f32_16x16x32_bf16 v[74:77], v[158:161], v[210:213], v[74:77]
	v_mfma_f32_16x16x32_bf16 v[70:73], v[150:153], v[218:221], v[70:73]
	v_mfma_f32_16x16x32_bf16 v[66:69], v[158:161], v[218:221], v[66:69]
	s_setprio 0
	s_barrier
	s_add_i32 s7, 0, 0x18000
	s_add_i32 s72, 0, 0x1c000
	v_add_u32_e32 v118, s7, v189
	v_add_u32_e32 v158, s72, v189
	ds_read_b128 v[106:109], v118
	ds_read_b128 v[110:113], v118 offset:1024
	ds_read_b128 v[114:117], v118 offset:2048
	ds_read_b128 v[118:121], v118 offset:3072
	ds_read_b128 v[146:149], v158
	ds_read_b128 v[150:153], v158 offset:1024
	ds_read_b128 v[154:157], v158 offset:2048
	ds_read_b128 v[158:161], v158 offset:3072
	s_add_u32 s10, s60, s0
	s_addc_u32 s11, s61, s1
	s_mov_b32 m0, s23
	v_lshl_add_u64 v[246:247], s[10:11], 0, v[162:163]
	ds_read_b128 v[172:175], v191 offset:32768
	ds_read_b128 v[176:179], v191 offset:33792
	ds_read_b128 v[180:183], v191 offset:34816
	ds_read_b128 v[192:195], v191 offset:35840
	ds_read_b128 v[196:199], v191 offset:36864
	ds_read_b128 v[210:213], v191 offset:37888
	ds_read_b128 v[214:217], v191 offset:38912
	ds_read_b128 v[218:221], v191 offset:39936
	global_load_lds_dwordx4 v[246:247], off
	v_lshl_add_u64 v[246:247], s[10:11], 0, v[164:165]
	s_mov_b32 m0, s26
	s_nop 0
	global_load_lds_dwordx4 v[246:247], off
	s_waitcnt vmcnt(8)
	s_waitcnt lgkmcnt(0)
	s_setprio 1
	s_barrier
	v_mfma_f32_16x16x32_bf16 v[62:65], v[106:109], v[172:175], v[62:65]
	v_mfma_f32_16x16x32_bf16 v[58:61], v[114:117], v[172:175], v[58:61]
	v_mfma_f32_16x16x32_bf16 v[54:57], v[106:109], v[180:183], v[54:57]
	v_mfma_f32_16x16x32_bf16 v[50:53], v[114:117], v[180:183], v[50:53]
	v_mfma_f32_16x16x32_bf16 v[46:49], v[106:109], v[196:199], v[46:49]
	v_mfma_f32_16x16x32_bf16 v[42:45], v[114:117], v[196:199], v[42:45]
	v_mfma_f32_16x16x32_bf16 v[38:41], v[106:109], v[214:217], v[38:41]
	v_mfma_f32_16x16x32_bf16 v[34:37], v[114:117], v[214:217], v[34:37]
	v_mfma_f32_16x16x32_bf16 v[62:65], v[110:113], v[176:179], v[62:65]
	v_mfma_f32_16x16x32_bf16 v[58:61], v[118:121], v[176:179], v[58:61]
	v_mfma_f32_16x16x32_bf16 v[54:57], v[110:113], v[192:195], v[54:57]
	v_mfma_f32_16x16x32_bf16 v[50:53], v[118:121], v[192:195], v[50:53]
	v_mfma_f32_16x16x32_bf16 v[46:49], v[110:113], v[210:213], v[46:49]
	v_mfma_f32_16x16x32_bf16 v[42:45], v[118:121], v[210:213], v[42:45]
	v_mfma_f32_16x16x32_bf16 v[38:41], v[110:113], v[218:221], v[38:41]
	v_mfma_f32_16x16x32_bf16 v[34:37], v[118:121], v[218:221], v[34:37]
	v_mfma_f32_16x16x32_bf16 v[142:145], v[146:149], v[172:175], v[142:145]
	v_mfma_f32_16x16x32_bf16 v[138:141], v[154:157], v[172:175], v[138:141]
	v_mfma_f32_16x16x32_bf16 v[134:137], v[146:149], v[180:183], v[134:137]
	v_mfma_f32_16x16x32_bf16 v[130:133], v[154:157], v[180:183], v[130:133]
	v_mfma_f32_16x16x32_bf16 v[126:129], v[146:149], v[196:199], v[126:129]
	v_mfma_f32_16x16x32_bf16 v[122:125], v[154:157], v[196:199], v[122:125]
	v_mfma_f32_16x16x32_bf16 v[102:105], v[146:149], v[214:217], v[102:105]
	v_mfma_f32_16x16x32_bf16 v[98:101], v[154:157], v[214:217], v[98:101]
	v_mfma_f32_16x16x32_bf16 v[142:145], v[150:153], v[176:179], v[142:145]
	v_mfma_f32_16x16x32_bf16 v[138:141], v[158:161], v[176:179], v[138:141]
	v_mfma_f32_16x16x32_bf16 v[134:137], v[150:153], v[192:195], v[134:137]
	v_mfma_f32_16x16x32_bf16 v[130:133], v[158:161], v[192:195], v[130:133]
	v_mfma_f32_16x16x32_bf16 v[126:129], v[150:153], v[210:213], v[126:129]
	v_mfma_f32_16x16x32_bf16 v[122:125], v[158:161], v[210:213], v[122:125]
	v_mfma_f32_16x16x32_bf16 v[102:105], v[150:153], v[218:221], v[102:105]
	v_mfma_f32_16x16x32_bf16 v[98:101], v[158:161], v[218:221], v[98:101]
	s_setprio 0
	s_barrier
	s_add_i32 s7, s7, s13
	v_lshl_add_u64 v[200:201], v[200:201], 0, s[14:15]
	s_mov_b32 m0, s7
	ds_read_b128 v[172:175], v191 offset:49152
	ds_read_b128 v[176:179], v191 offset:50176
	ds_read_b128 v[180:183], v191 offset:51200
	ds_read_b128 v[192:195], v191 offset:52224
	ds_read_b128 v[196:199], v191 offset:53248
	ds_read_b128 v[210:213], v191 offset:54272
	ds_read_b128 v[214:217], v191 offset:55296
	ds_read_b128 v[218:221], v191 offset:56320
	global_load_lds_dwordx4 v[200:201], off
	v_lshl_add_u64 v[200:201], v[222:223], 0, s[14:15]
	s_add_i32 m0, s7, 0x2000
	s_add_i32 s7, s72, s13
	global_load_lds_dwordx4 v[200:201], off
	v_lshl_add_u64 v[200:201], v[224:225], 0, s[14:15]
	s_mov_b32 m0, s7
	s_nop 0
	global_load_lds_dwordx4 v[200:201], off
	v_lshl_add_u64 v[200:201], v[226:227], 0, s[14:15]
	s_add_i32 m0, s7, 0x2000
	s_nop 0
	global_load_lds_dwordx4 v[200:201], off
	v_lshl_add_u64 v[200:201], v[228:229], 0, s[14:15]
	s_mov_b32 m0, s27
	s_nop 0
	global_load_lds_dwordx4 v[200:201], off
	v_lshl_add_u64 v[200:201], v[230:231], 0, s[14:15]
	s_mov_b32 m0, s28
	s_nop 0
	global_load_lds_dwordx4 v[200:201], off
	s_waitcnt vmcnt(8)
	s_waitcnt lgkmcnt(0)
	s_setprio 1
	s_barrier
	v_mfma_f32_16x16x32_bf16 v[30:33], v[106:109], v[172:175], v[30:33]
	v_mfma_f32_16x16x32_bf16 v[26:29], v[114:117], v[172:175], v[26:29]
	v_mfma_f32_16x16x32_bf16 v[22:25], v[106:109], v[180:183], v[22:25]
	v_mfma_f32_16x16x32_bf16 v[18:21], v[114:117], v[180:183], v[18:21]
	v_mfma_f32_16x16x32_bf16 v[14:17], v[106:109], v[196:199], v[14:17]
	v_mfma_f32_16x16x32_bf16 v[10:13], v[114:117], v[196:199], v[10:13]
	v_mfma_f32_16x16x32_bf16 v[6:9], v[106:109], v[214:217], v[6:9]
	v_mfma_f32_16x16x32_bf16 v[2:5], v[114:117], v[214:217], v[2:5]
	v_mfma_f32_16x16x32_bf16 v[30:33], v[110:113], v[176:179], v[30:33]
	v_mfma_f32_16x16x32_bf16 v[26:29], v[118:121], v[176:179], v[26:29]
	v_mfma_f32_16x16x32_bf16 v[22:25], v[110:113], v[192:195], v[22:25]
	v_mfma_f32_16x16x32_bf16 v[18:21], v[118:121], v[192:195], v[18:21]
	v_mfma_f32_16x16x32_bf16 v[14:17], v[110:113], v[210:213], v[14:17]
	v_mfma_f32_16x16x32_bf16 v[10:13], v[118:121], v[210:213], v[10:13]
	v_mfma_f32_16x16x32_bf16 v[6:9], v[110:113], v[218:221], v[6:9]
	v_mfma_f32_16x16x32_bf16 v[2:5], v[118:121], v[218:221], v[2:5]
	v_mfma_f32_16x16x32_bf16 v[94:97], v[146:149], v[172:175], v[94:97]
	v_mfma_f32_16x16x32_bf16 v[90:93], v[154:157], v[172:175], v[90:93]
	v_mfma_f32_16x16x32_bf16 v[86:89], v[146:149], v[180:183], v[86:89]
	v_mfma_f32_16x16x32_bf16 v[82:85], v[154:157], v[180:183], v[82:85]
	v_mfma_f32_16x16x32_bf16 v[78:81], v[146:149], v[196:199], v[78:81]
	v_mfma_f32_16x16x32_bf16 v[74:77], v[154:157], v[196:199], v[74:77]
	v_mfma_f32_16x16x32_bf16 v[70:73], v[146:149], v[214:217], v[70:73]
	v_mfma_f32_16x16x32_bf16 v[66:69], v[154:157], v[214:217], v[66:69]
	v_mfma_f32_16x16x32_bf16 v[94:97], v[150:153], v[176:179], v[94:97]
	v_mfma_f32_16x16x32_bf16 v[90:93], v[158:161], v[176:179], v[90:93]
	v_mfma_f32_16x16x32_bf16 v[86:89], v[150:153], v[192:195], v[86:89]
	v_mfma_f32_16x16x32_bf16 v[82:85], v[158:161], v[192:195], v[82:85]
	v_mfma_f32_16x16x32_bf16 v[78:81], v[150:153], v[210:213], v[78:81]
	v_mfma_f32_16x16x32_bf16 v[74:77], v[158:161], v[210:213], v[74:77]
	v_mfma_f32_16x16x32_bf16 v[70:73], v[150:153], v[218:221], v[70:73]
	v_mfma_f32_16x16x32_bf16 v[66:69], v[158:161], v[218:221], v[66:69]
	s_setprio 0
	s_barrier
	s_add_u32 s38, s38, 0x100
	s_addc_u32 s39, s39, 0
	s_add_u32 s62, s62, 0x100
	s_addc_u32 s63, s63, 0
	s_cmp_ge_i32 s71, s29
	s_mov_b32 s60, s71
	s_cbranch_scc0 .LBB0_622
	v_readlane_b32 s72, v255, 33
	v_readlane_b32 s73, v255, 34

.LBB0_1637:
	s_add_i32 s71, s70, 2
	s_add_u32 s7, s48, 0x80
	s_addc_u32 s10, s49, 0
	s_cmp_eq_u32 s60, s70
	s_cselect_b32 s51, s39, s10
	s_cselect_b32 s50, s38, s7
	s_cselect_b32 s53, s47, s69
	s_cselect_b32 s52, s46, s68
	s_add_i32 s7, 0, 0x10000
	v_add_u32_e32 v130, s7, v215
	s_add_i32 s70, 0, 0x14000
	ds_read_b128 v[134:137], v130
	ds_read_b128 v[138:141], v130 offset:1024
	ds_read_b128 v[142:145], v130 offset:2048
	ds_read_b128 v[146:149], v130 offset:3072
	v_add_u32_e32 v130, s70, v215
	ds_read_b128 v[150:153], v130
	ds_read_b128 v[154:157], v130 offset:1024
	ds_read_b128 v[158:161], v130 offset:2048
	ds_read_b128 v[162:165], v130 offset:3072
	v_lshl_add_u64 v[130:131], s[48:49], 0, v[200:201]
	s_add_i32 m0, s23, 0xc000
	ds_read_b128 v[166:169], v216
	ds_read_b128 v[170:173], v216 offset:1024
	ds_read_b128 v[174:177], v216 offset:2048
	ds_read_b128 v[178:181], v216 offset:3072
	ds_read_b128 v[182:185], v216 offset:4096
	ds_read_b128 v[186:189], v216 offset:5120
	ds_read_b128 v[218:221], v216 offset:6144
	ds_read_b128 v[222:225], v216 offset:7168
	global_load_lds_dwordx4 v[130:131], off
	v_lshl_add_u64 v[130:131], s[48:49], 0, v[210:211]
	s_add_i32 m0, s23, 0xe000
	s_nop 0
	global_load_lds_dwordx4 v[130:131], off
	s_waitcnt vmcnt(8)
	s_waitcnt lgkmcnt(0)
	s_setprio 1
	s_barrier
	v_mfma_f32_16x16x128_f8f6f4 v[126:129], v[134:141], v[166:173], v[126:129]
	v_mfma_f32_16x16x128_f8f6f4 v[122:125], v[142:149], v[166:173], v[122:125]
	v_mfma_f32_16x16x128_f8f6f4 v[110:113], v[134:141], v[174:181], v[110:113]
	v_mfma_f32_16x16x128_f8f6f4 v[106:109], v[142:149], v[174:181], v[106:109]
	v_mfma_f32_16x16x128_f8f6f4 v[94:97], v[134:141], v[182:189], v[94:97]
	v_mfma_f32_16x16x128_f8f6f4 v[90:93], v[142:149], v[182:189], v[90:93]
	v_mfma_f32_16x16x128_f8f6f4 v[78:81], v[134:141], v[218:225], v[78:81]
	v_mfma_f32_16x16x128_f8f6f4 v[74:77], v[142:149], v[218:225], v[74:77]
	v_mfma_f32_16x16x128_f8f6f4 v[118:121], v[150:157], v[166:173], v[118:121]
	v_mfma_f32_16x16x128_f8f6f4 v[114:117], v[158:165], v[166:173], v[114:117]
	v_mfma_f32_16x16x128_f8f6f4 v[102:105], v[150:157], v[174:181], v[102:105]
	v_mfma_f32_16x16x128_f8f6f4 v[98:101], v[158:165], v[174:181], v[98:101]
	v_mfma_f32_16x16x128_f8f6f4 v[86:89], v[150:157], v[182:189], v[86:89]
	v_mfma_f32_16x16x128_f8f6f4 v[82:85], v[158:165], v[182:189], v[82:85]
	v_mfma_f32_16x16x128_f8f6f4 v[70:73], v[150:157], v[218:225], v[70:73]
	v_mfma_f32_16x16x128_f8f6f4 v[66:69], v[158:165], v[218:225], v[66:69]
	s_setprio 0
	s_barrier
	s_add_i32 s7, s7, s17
	v_lshl_add_u64 v[130:131], s[52:53], 0, v[0:1]
	s_mov_b32 m0, s7
	ds_read_b128 v[166:169], v216 offset:16384
	ds_read_b128 v[170:173], v216 offset:17408
	ds_read_b128 v[174:177], v216 offset:18432
	ds_read_b128 v[178:181], v216 offset:19456
	ds_read_b128 v[182:185], v216 offset:20480
	ds_read_b128 v[186:189], v216 offset:21504
	ds_read_b128 v[218:221], v216 offset:22528
	ds_read_b128 v[222:225], v216 offset:23552
	global_load_lds_dwordx4 v[130:131], off
	s_add_i32 m0, s7, 0x2000
	s_add_u32 s10, s52, s0
	v_lshl_add_u64 v[132:133], s[52:53], 0, v[198:199]
	s_addc_u32 s11, s53, s1
	s_add_i32 s7, s70, s17
	global_load_lds_dwordx4 v[132:133], off
	v_lshl_add_u64 v[190:191], s[10:11], 0, v[0:1]
	s_mov_b32 m0, s7
	v_lshl_add_u64 v[192:193], s[10:11], 0, v[198:199]
	global_load_lds_dwordx4 v[190:191], off
	s_add_i32 m0, s7, 0x2000
	v_lshl_add_u64 v[212:213], s[50:51], 0, v[194:195]
	global_load_lds_dwordx4 v[192:193], off
	s_mov_b32 m0, s23
	v_lshl_add_u64 v[226:227], s[50:51], 0, v[196:197]
	global_load_lds_dwordx4 v[212:213], off
	s_mov_b32 m0, s26
	s_nop 0
	global_load_lds_dwordx4 v[226:227], off
	s_waitcnt vmcnt(8)
	s_waitcnt lgkmcnt(0)
	s_setprio 1
	s_barrier
	v_mfma_f32_16x16x128_f8f6f4 v[62:65], v[134:141], v[166:173], v[62:65]
	v_mfma_f32_16x16x128_f8f6f4 v[58:61], v[142:149], v[166:173], v[58:61]
	v_mfma_f32_16x16x128_f8f6f4 v[46:49], v[134:141], v[174:181], v[46:49]
	v_mfma_f32_16x16x128_f8f6f4 v[42:45], v[142:149], v[174:181], v[42:45]
	v_mfma_f32_16x16x128_f8f6f4 v[30:33], v[134:141], v[182:189], v[30:33]
	v_mfma_f32_16x16x128_f8f6f4 v[26:29], v[142:149], v[182:189], v[26:29]
	v_mfma_f32_16x16x128_f8f6f4 v[14:17], v[134:141], v[218:225], v[14:17]
	v_mfma_f32_16x16x128_f8f6f4 v[10:13], v[142:149], v[218:225], v[10:13]
	v_mfma_f32_16x16x128_f8f6f4 v[54:57], v[150:157], v[166:173], v[54:57]
	v_mfma_f32_16x16x128_f8f6f4 v[50:53], v[158:165], v[166:173], v[50:53]
	v_mfma_f32_16x16x128_f8f6f4 v[38:41], v[150:157], v[174:181], v[38:41]
	v_mfma_f32_16x16x128_f8f6f4 v[34:37], v[158:165], v[174:181], v[34:37]
	v_mfma_f32_16x16x128_f8f6f4 v[22:25], v[150:157], v[182:189], v[22:25]
	v_mfma_f32_16x16x128_f8f6f4 v[18:21], v[158:165], v[182:189], v[18:21]
	v_mfma_f32_16x16x128_f8f6f4 v[6:9], v[150:157], v[218:225], v[6:9]
	v_mfma_f32_16x16x128_f8f6f4 v[2:5], v[158:165], v[218:225], v[2:5]
	s_setprio 0
	s_barrier
	s_add_i32 s7, 0, 0x18000
	s_add_i32 s52, 0, 0x1c000
	v_add_u32_e32 v146, s7, v215
	v_add_u32_e32 v162, s52, v215
	ds_read_b128 v[134:137], v146
	ds_read_b128 v[138:141], v146 offset:1024
	ds_read_b128 v[142:145], v146 offset:2048
	ds_read_b128 v[146:149], v146 offset:3072
	ds_read_b128 v[150:153], v162
	ds_read_b128 v[154:157], v162 offset:1024
	ds_read_b128 v[158:161], v162 offset:2048
	ds_read_b128 v[162:165], v162 offset:3072
	s_add_u32 s10, s50, s0
	s_addc_u32 s11, s51, s1
	s_mov_b32 m0, s27
	v_lshl_add_u64 v[228:229], s[10:11], 0, v[194:195]
	ds_read_b128 v[166:169], v216 offset:32768
	ds_read_b128 v[170:173], v216 offset:33792
	ds_read_b128 v[174:177], v216 offset:34816
	ds_read_b128 v[178:181], v216 offset:35840
	ds_read_b128 v[182:185], v216 offset:36864
	ds_read_b128 v[186:189], v216 offset:37888
	ds_read_b128 v[218:221], v216 offset:38912
	ds_read_b128 v[222:225], v216 offset:39936
	global_load_lds_dwordx4 v[228:229], off
	v_lshl_add_u64 v[228:229], s[10:11], 0, v[196:197]
	s_mov_b32 m0, s54
	s_nop 0
	global_load_lds_dwordx4 v[228:229], off
	s_waitcnt vmcnt(8)
	s_waitcnt lgkmcnt(0)
	s_setprio 1
	s_barrier
	v_mfma_f32_16x16x128_f8f6f4 v[126:129], v[134:141], v[166:173], v[126:129]
	v_mfma_f32_16x16x128_f8f6f4 v[122:125], v[142:149], v[166:173], v[122:125]
	v_mfma_f32_16x16x128_f8f6f4 v[110:113], v[134:141], v[174:181], v[110:113]
	v_mfma_f32_16x16x128_f8f6f4 v[106:109], v[142:149], v[174:181], v[106:109]
	v_mfma_f32_16x16x128_f8f6f4 v[94:97], v[134:141], v[182:189], v[94:97]
	v_mfma_f32_16x16x128_f8f6f4 v[90:93], v[142:149], v[182:189], v[90:93]
	v_mfma_f32_16x16x128_f8f6f4 v[78:81], v[134:141], v[218:225], v[78:81]
	v_mfma_f32_16x16x128_f8f6f4 v[74:77], v[142:149], v[218:225], v[74:77]
	v_mfma_f32_16x16x128_f8f6f4 v[118:121], v[150:157], v[166:173], v[118:121]
	v_mfma_f32_16x16x128_f8f6f4 v[114:117], v[158:165], v[166:173], v[114:117]
	v_mfma_f32_16x16x128_f8f6f4 v[102:105], v[150:157], v[174:181], v[102:105]
	v_mfma_f32_16x16x128_f8f6f4 v[98:101], v[158:165], v[174:181], v[98:101]
	v_mfma_f32_16x16x128_f8f6f4 v[86:89], v[150:157], v[182:189], v[86:89]
	v_mfma_f32_16x16x128_f8f6f4 v[82:85], v[158:165], v[182:189], v[82:85]
	v_mfma_f32_16x16x128_f8f6f4 v[70:73], v[150:157], v[218:225], v[70:73]
	v_mfma_f32_16x16x128_f8f6f4 v[66:69], v[158:165], v[218:225], v[66:69]
	s_setprio 0
	s_barrier
	s_add_i32 s7, s7, s17
	v_lshl_add_u64 v[130:131], v[130:131], 0, s[14:15]
	s_mov_b32 m0, s7
	ds_read_b128 v[166:169], v216 offset:49152
	ds_read_b128 v[170:173], v216 offset:50176
	ds_read_b128 v[174:177], v216 offset:51200
	ds_read_b128 v[178:181], v216 offset:52224
	ds_read_b128 v[182:185], v216 offset:53248
	ds_read_b128 v[186:189], v216 offset:54272
	ds_read_b128 v[218:221], v216 offset:55296
	ds_read_b128 v[222:225], v216 offset:56320
	global_load_lds_dwordx4 v[130:131], off
	v_lshl_add_u64 v[130:131], v[132:133], 0, s[14:15]
	s_add_i32 m0, s7, 0x2000
	s_add_i32 s7, s52, s17
	global_load_lds_dwordx4 v[130:131], off
	v_lshl_add_u64 v[130:131], v[190:191], 0, s[14:15]
	s_mov_b32 m0, s7
	s_nop 0
	global_load_lds_dwordx4 v[130:131], off
	v_lshl_add_u64 v[130:131], v[192:193], 0, s[14:15]
	s_add_i32 m0, s7, 0x2000
	s_nop 0
	global_load_lds_dwordx4 v[130:131], off
	v_lshl_add_u64 v[130:131], v[212:213], 0, s[14:15]
	s_mov_b32 m0, s58
	s_nop 0
	global_load_lds_dwordx4 v[130:131], off
	v_lshl_add_u64 v[130:131], v[226:227], 0, s[14:15]
	s_mov_b32 m0, s59
	s_nop 0
	global_load_lds_dwordx4 v[130:131], off
	s_waitcnt vmcnt(8)
	s_waitcnt lgkmcnt(0)
	s_setprio 1
	s_barrier
	v_mfma_f32_16x16x128_f8f6f4 v[62:65], v[134:141], v[166:173], v[62:65]
	v_mfma_f32_16x16x128_f8f6f4 v[58:61], v[142:149], v[166:173], v[58:61]
	v_mfma_f32_16x16x128_f8f6f4 v[46:49], v[134:141], v[174:181], v[46:49]
	v_mfma_f32_16x16x128_f8f6f4 v[42:45], v[142:149], v[174:181], v[42:45]
	v_mfma_f32_16x16x128_f8f6f4 v[30:33], v[134:141], v[182:189], v[30:33]
	v_mfma_f32_16x16x128_f8f6f4 v[26:29], v[142:149], v[182:189], v[26:29]
	v_mfma_f32_16x16x128_f8f6f4 v[14:17], v[134:141], v[218:225], v[14:17]
	v_mfma_f32_16x16x128_f8f6f4 v[10:13], v[142:149], v[218:225], v[10:13]
	v_mfma_f32_16x16x128_f8f6f4 v[54:57], v[150:157], v[166:173], v[54:57]
	v_mfma_f32_16x16x128_f8f6f4 v[50:53], v[158:165], v[166:173], v[50:53]
	v_mfma_f32_16x16x128_f8f6f4 v[38:41], v[150:157], v[174:181], v[38:41]
	v_mfma_f32_16x16x128_f8f6f4 v[34:37], v[158:165], v[174:181], v[34:37]
	v_mfma_f32_16x16x128_f8f6f4 v[22:25], v[150:157], v[182:189], v[22:25]
	v_mfma_f32_16x16x128_f8f6f4 v[18:21], v[158:165], v[182:189], v[18:21]
	v_mfma_f32_16x16x128_f8f6f4 v[6:9], v[150:157], v[218:225], v[6:9]
	v_mfma_f32_16x16x128_f8f6f4 v[2:5], v[158:165], v[218:225], v[2:5]
	s_setprio 0
	s_barrier
	s_addk_i32 s8, 0x400
	s_add_u32 s48, s48, 0x100
	s_addc_u32 s49, s49, 0
	s_add_u32 s68, s68, 0x100
	s_addc_u32 s69, s69, 0
	s_cmp_ge_i32 s71, s55
	s_cbranch_scc1 .LBB0_1640
	s_mov_b32 s70, s71
	s_cmp_lt_i32 s70, 16
	s_cbranch_scc1 .LBB0_1633

.LBB0_1722:
	s_add_i32 vcc_hi, s66, 2
	s_add_u32 s10, s64, 0x80
	s_addc_u32 s11, s65, 0
	s_add_i32 s7, 0, 0x10000
	s_cmp_eq_u32 s74, s66
	s_cselect_b32 s67, s39, s11
	s_cselect_b32 s66, s38, s10
	s_cselect_b32 s69, s63, vcc_lo
	s_cselect_b32 s68, s62, s97
	s_add_i32 s10, 0, 0x14000
	v_add_u32_e32 v2, s7, v228
	v_add_u32_e32 v6, s10, v228
	ds_read_b128 v[26:29], v2
	ds_read_b128 v[30:33], v2 offset:1024
	ds_read_b128 v[18:21], v2 offset:2048
	ds_read_b128 v[22:25], v2 offset:3072
	ds_read_b128 v[10:13], v6
	ds_read_b128 v[14:17], v6 offset:1024
	s_waitcnt lgkmcnt(0)
	ds_read_b128 v[2:5], v6 offset:2048
	ds_read_b128 v[6:9], v6 offset:3072
	v_lshl_add_u64 v[196:197], s[64:65], 0, v[168:169]
	s_add_i32 m0, s16, 0xc000
	ds_read_b128 v[172:175], v229
	ds_read_b128 v[176:179], v229 offset:1024
	ds_read_b128 v[180:183], v229 offset:2048
	ds_read_b128 v[184:187], v229 offset:3072
	ds_read_b128 v[188:191], v229 offset:4096
	ds_read_b128 v[192:195], v229 offset:5120
	ds_read_b128 v[210:213], v229 offset:6144
	ds_read_b128 v[214:217], v229 offset:7168
	global_load_lds_dwordx4 v[196:197], off
	v_lshl_add_u64 v[196:197], s[64:65], 0, v[170:171]
	s_add_i32 m0, s16, 0xe000
	s_nop 0
	global_load_lds_dwordx4 v[196:197], off
	s_waitcnt vmcnt(8)
	s_waitcnt lgkmcnt(0)
	s_setprio 1
	s_barrier
	v_mfma_f32_16x16x128_f8f6f4 v[158:161], v[26:33], v[172:179], v[158:161]
	v_mfma_f32_16x16x128_f8f6f4 v[154:157], v[18:25], v[172:179], v[154:157]
	v_mfma_f32_16x16x128_f8f6f4 v[150:153], v[26:33], v[180:187], v[150:153]
	v_mfma_f32_16x16x128_f8f6f4 v[146:149], v[18:25], v[180:187], v[146:149]
	v_mfma_f32_16x16x128_f8f6f4 v[138:141], v[26:33], v[188:195], v[138:141]
	v_mfma_f32_16x16x128_f8f6f4 v[130:133], v[18:25], v[188:195], v[130:133]
	v_mfma_f32_16x16x128_f8f6f4 v[122:125], v[26:33], v[210:217], v[122:125]
	v_mfma_f32_16x16x128_f8f6f4 v[114:117], v[18:25], v[210:217], v[114:117]
	v_mfma_f32_16x16x128_f8f6f4 v[142:145], v[10:17], v[172:179], v[142:145]
	v_mfma_f32_16x16x128_f8f6f4 v[134:137], v[2:9], v[172:179], v[134:137]
	v_mfma_f32_16x16x128_f8f6f4 v[126:129], v[10:17], v[180:187], v[126:129]
	v_mfma_f32_16x16x128_f8f6f4 v[118:121], v[2:9], v[180:187], v[118:121]
	v_mfma_f32_16x16x128_f8f6f4 v[110:113], v[10:17], v[188:195], v[110:113]
	v_mfma_f32_16x16x128_f8f6f4 v[106:109], v[2:9], v[188:195], v[106:109]
	v_mfma_f32_16x16x128_f8f6f4 v[102:105], v[10:17], v[210:217], v[102:105]
	v_mfma_f32_16x16x128_f8f6f4 v[98:101], v[2:9], v[210:217], v[98:101]
	s_setprio 0
	s_barrier
	s_add_i32 s7, s7, s13
	v_lshl_add_u64 v[172:173], s[68:69], 0, v[0:1]
	s_mov_b32 m0, s7
	ds_read_b128 v[184:187], v229 offset:16384
	ds_read_b128 v[188:191], v229 offset:17408
	ds_read_b128 v[192:195], v229 offset:18432
	ds_read_b128 v[196:199], v229 offset:19456
	ds_read_b128 v[210:213], v229 offset:20480
	ds_read_b128 v[214:217], v229 offset:21504
	ds_read_b128 v[218:221], v229 offset:22528
	ds_read_b128 v[222:225], v229 offset:23552
	global_load_lds_dwordx4 v[172:173], off
	s_add_i32 m0, s7, 0x2000
	v_lshl_add_u64 v[174:175], s[68:69], 0, v[166:167]
	s_add_u32 s68, s68, s28
	s_addc_u32 s69, s69, s29
	s_add_i32 s7, s10, s13
	global_load_lds_dwordx4 v[174:175], off
	v_lshl_add_u64 v[176:177], s[68:69], 0, v[0:1]
	s_mov_b32 m0, s7
	v_lshl_add_u64 v[178:179], s[68:69], 0, v[166:167]
	global_load_lds_dwordx4 v[176:177], off
	s_add_i32 m0, s7, 0x2000
	v_lshl_add_u64 v[180:181], s[66:67], 0, v[162:163]
	global_load_lds_dwordx4 v[178:179], off
	s_mov_b32 m0, s16
	v_lshl_add_u64 v[182:183], s[66:67], 0, v[164:165]
	global_load_lds_dwordx4 v[180:181], off
	s_mov_b32 m0, s17
	s_nop 0
	global_load_lds_dwordx4 v[182:183], off
	s_waitcnt vmcnt(8)
	s_waitcnt lgkmcnt(0)
	s_setprio 1
	s_barrier
	v_mfma_f32_16x16x128_f8f6f4 v[94:97], v[26:33], v[184:191], v[94:97]
	v_mfma_f32_16x16x128_f8f6f4 v[90:93], v[18:25], v[184:191], v[90:93]
	v_mfma_f32_16x16x128_f8f6f4 v[86:89], v[26:33], v[192:199], v[86:89]
	v_mfma_f32_16x16x128_f8f6f4 v[82:85], v[18:25], v[192:199], v[82:85]
	v_mfma_f32_16x16x128_f8f6f4 v[74:77], v[26:33], v[210:217], v[74:77]
	v_mfma_f32_16x16x128_f8f6f4 v[66:69], v[18:25], v[210:217], v[66:69]
	v_mfma_f32_16x16x128_f8f6f4 v[58:61], v[26:33], v[218:225], v[58:61]
	v_mfma_f32_16x16x128_f8f6f4 v[50:53], v[18:25], v[218:225], v[50:53]
	v_mfma_f32_16x16x128_f8f6f4 v[78:81], v[10:17], v[184:191], v[78:81]
	v_mfma_f32_16x16x128_f8f6f4 v[70:73], v[2:9], v[184:191], v[70:73]
	v_mfma_f32_16x16x128_f8f6f4 v[62:65], v[10:17], v[192:199], v[62:65]
	v_mfma_f32_16x16x128_f8f6f4 v[54:57], v[2:9], v[192:199], v[54:57]
	v_mfma_f32_16x16x128_f8f6f4 v[46:49], v[10:17], v[210:217], v[46:49]
	v_mfma_f32_16x16x128_f8f6f4 v[42:45], v[2:9], v[210:217], v[42:45]
	v_mfma_f32_16x16x128_f8f6f4 v[38:41], v[10:17], v[218:225], v[38:41]
	v_mfma_f32_16x16x128_f8f6f4 v[34:37], v[2:9], v[218:225], v[34:37]
	s_setprio 0
	s_barrier
	s_add_i32 s7, 0, 0x18000
	s_add_i32 s68, 0, 0x1c000
	v_add_u32_e32 v14, s7, v228
	v_add_u32_e32 v30, s68, v228
	ds_read_b128 v[2:5], v14
	ds_read_b128 v[6:9], v14 offset:1024
	ds_read_b128 v[10:13], v14 offset:2048
	ds_read_b128 v[14:17], v14 offset:3072
	ds_read_b128 v[18:21], v30
	ds_read_b128 v[22:25], v30 offset:1024
	ds_read_b128 v[26:29], v30 offset:2048
	ds_read_b128 v[30:33], v30 offset:3072
	s_add_u32 s10, s66, s28
	s_addc_u32 s11, s67, s29
	s_mov_b32 m0, s23
	v_lshl_add_u64 v[200:201], s[10:11], 0, v[162:163]
	ds_read_b128 v[184:187], v229 offset:32768
	ds_read_b128 v[188:191], v229 offset:33792
	ds_read_b128 v[192:195], v229 offset:34816
	ds_read_b128 v[196:199], v229 offset:35840
	ds_read_b128 v[210:213], v229 offset:36864
	ds_read_b128 v[214:217], v229 offset:37888
	ds_read_b128 v[218:221], v229 offset:38912
	ds_read_b128 v[222:225], v229 offset:39936
	global_load_lds_dwordx4 v[200:201], off
	v_lshl_add_u64 v[200:201], s[10:11], 0, v[164:165]
	s_mov_b32 m0, s26
	s_nop 0
	global_load_lds_dwordx4 v[200:201], off
	s_waitcnt vmcnt(8)
	s_waitcnt lgkmcnt(0)
	s_setprio 1
	s_barrier
	v_mfma_f32_16x16x128_f8f6f4 v[158:161], v[2:9], v[184:191], v[158:161]
	v_mfma_f32_16x16x128_f8f6f4 v[154:157], v[10:17], v[184:191], v[154:157]
	v_mfma_f32_16x16x128_f8f6f4 v[150:153], v[2:9], v[192:199], v[150:153]
	v_mfma_f32_16x16x128_f8f6f4 v[146:149], v[10:17], v[192:199], v[146:149]
	v_mfma_f32_16x16x128_f8f6f4 v[138:141], v[2:9], v[210:217], v[138:141]
	v_mfma_f32_16x16x128_f8f6f4 v[130:133], v[10:17], v[210:217], v[130:133]
	v_mfma_f32_16x16x128_f8f6f4 v[122:125], v[2:9], v[218:225], v[122:125]
	v_mfma_f32_16x16x128_f8f6f4 v[114:117], v[10:17], v[218:225], v[114:117]
	v_mfma_f32_16x16x128_f8f6f4 v[142:145], v[18:25], v[184:191], v[142:145]
	v_mfma_f32_16x16x128_f8f6f4 v[134:137], v[26:33], v[184:191], v[134:137]
	v_mfma_f32_16x16x128_f8f6f4 v[126:129], v[18:25], v[192:199], v[126:129]
	v_mfma_f32_16x16x128_f8f6f4 v[118:121], v[26:33], v[192:199], v[118:121]
	v_mfma_f32_16x16x128_f8f6f4 v[110:113], v[18:25], v[210:217], v[110:113]
	v_mfma_f32_16x16x128_f8f6f4 v[106:109], v[26:33], v[210:217], v[106:109]
	v_mfma_f32_16x16x128_f8f6f4 v[102:105], v[18:25], v[218:225], v[102:105]
	v_mfma_f32_16x16x128_f8f6f4 v[98:101], v[26:33], v[218:225], v[98:101]
	s_setprio 0
	s_barrier
	s_add_i32 s7, s7, s13
	v_lshl_add_u64 v[172:173], v[172:173], 0, s[14:15]
	s_mov_b32 m0, s7
	ds_read_b128 v[184:187], v229 offset:49152
	ds_read_b128 v[188:191], v229 offset:50176
	ds_read_b128 v[192:195], v229 offset:51200
	ds_read_b128 v[196:199], v229 offset:52224
	ds_read_b128 v[210:213], v229 offset:53248
	ds_read_b128 v[214:217], v229 offset:54272
	ds_read_b128 v[218:221], v229 offset:55296
	ds_read_b128 v[222:225], v229 offset:56320
	global_load_lds_dwordx4 v[172:173], off
	v_lshl_add_u64 v[172:173], v[174:175], 0, s[14:15]
	s_add_i32 m0, s7, 0x2000
	s_add_i32 s7, s68, s13
	global_load_lds_dwordx4 v[172:173], off
	v_lshl_add_u64 v[172:173], v[176:177], 0, s[14:15]
	s_mov_b32 m0, s7
	s_nop 0
	global_load_lds_dwordx4 v[172:173], off
	v_lshl_add_u64 v[172:173], v[178:179], 0, s[14:15]
	s_add_i32 m0, s7, 0x2000
	s_nop 0
	global_load_lds_dwordx4 v[172:173], off
	v_lshl_add_u64 v[172:173], v[180:181], 0, s[14:15]
	s_mov_b32 m0, s27
	s_nop 0
	global_load_lds_dwordx4 v[172:173], off
	v_lshl_add_u64 v[172:173], v[182:183], 0, s[14:15]
	s_mov_b32 m0, s70
	s_nop 0
	global_load_lds_dwordx4 v[172:173], off
	s_waitcnt vmcnt(8)
	s_waitcnt lgkmcnt(0)
	s_setprio 1
	s_barrier
	v_mfma_f32_16x16x128_f8f6f4 v[94:97], v[2:9], v[184:191], v[94:97]
	v_mfma_f32_16x16x128_f8f6f4 v[90:93], v[10:17], v[184:191], v[90:93]
	v_mfma_f32_16x16x128_f8f6f4 v[86:89], v[2:9], v[192:199], v[86:89]
	v_mfma_f32_16x16x128_f8f6f4 v[82:85], v[10:17], v[192:199], v[82:85]
	v_mfma_f32_16x16x128_f8f6f4 v[74:77], v[2:9], v[210:217], v[74:77]
	v_mfma_f32_16x16x128_f8f6f4 v[66:69], v[10:17], v[210:217], v[66:69]
	v_mfma_f32_16x16x128_f8f6f4 v[58:61], v[2:9], v[218:225], v[58:61]
	v_mfma_f32_16x16x128_f8f6f4 v[50:53], v[10:17], v[218:225], v[50:53]
	v_mfma_f32_16x16x128_f8f6f4 v[78:81], v[18:25], v[184:191], v[78:81]
	v_mfma_f32_16x16x128_f8f6f4 v[70:73], v[26:33], v[184:191], v[70:73]
	v_mfma_f32_16x16x128_f8f6f4 v[62:65], v[18:25], v[192:199], v[62:65]
	v_mfma_f32_16x16x128_f8f6f4 v[54:57], v[26:33], v[192:199], v[54:57]
	v_mfma_f32_16x16x128_f8f6f4 v[46:49], v[18:25], v[210:217], v[46:49]
	v_mfma_f32_16x16x128_f8f6f4 v[42:45], v[26:33], v[210:217], v[42:45]
	v_mfma_f32_16x16x128_f8f6f4 v[38:41], v[18:25], v[218:225], v[38:41]
	v_mfma_f32_16x16x128_f8f6f4 v[34:37], v[26:33], v[218:225], v[34:37]
	s_setprio 0
	s_barrier
	s_add_u32 s64, s64, 0x100
	s_addc_u32 s65, s65, 0
	s_add_u32 s97, s97, 0x100
	s_addc_u32 vcc_lo, vcc_lo, 0
	s_cmp_ge_i32 vcc_hi, s71
	s_mov_b32 s66, vcc_hi
	s_cbranch_scc0 .LBB0_1722
	v_pk_mul_f32 v[214:215], v[160:161], s[18:19] op_sel_hi:[1,0]
	v_pk_mul_f32 v[216:217], v[158:159], s[18:19] op_sel_hi:[1,0]
	v_pk_mul_f32 v[220:221], v[156:157], s[18:19] op_sel_hi:[1,0]
	v_pk_mul_f32 v[218:219], v[154:155], s[18:19] op_sel_hi:[1,0]
	v_pk_mul_f32 v[200:201], v[144:145], s[18:19] op_sel_hi:[1,0]
	v_pk_mul_f32 v[198:199], v[142:143], s[18:19] op_sel_hi:[1,0]
	v_pk_mul_f32 v[212:213], v[136:137], s[18:19] op_sel_hi:[1,0]
	v_pk_mul_f32 v[210:211], v[134:135], s[18:19] op_sel_hi:[1,0]
	v_pk_mul_f32 v[190:191], v[152:153], s[18:19] op_sel_hi:[1,0]
	v_pk_mul_f32 v[192:193], v[150:151], s[18:19] op_sel_hi:[1,0]
	v_pk_mul_f32 v[194:195], v[148:149], s[18:19] op_sel_hi:[1,0]
	v_pk_mul_f32 v[196:197], v[146:147], s[18:19] op_sel_hi:[1,0]
	v_pk_mul_f32 v[180:181], v[128:129], s[18:19] op_sel_hi:[1,0]
	v_pk_mul_f32 v[182:183], v[126:127], s[18:19] op_sel_hi:[1,0]
	v_pk_mul_f32 v[184:185], v[120:121], s[18:19] op_sel_hi:[1,0]
	v_pk_mul_f32 v[186:187], v[118:119], s[18:19] op_sel_hi:[1,0]
	v_pk_mul_f32 v[172:173], v[140:141], s[18:19] op_sel_hi:[1,0]
	v_pk_mul_f32 v[174:175], v[138:139], s[18:19] op_sel_hi:[1,0]
	v_pk_mul_f32 v[176:177], v[132:133], s[18:19] op_sel_hi:[1,0]
	v_pk_mul_f32 v[178:179], v[130:131], s[18:19] op_sel_hi:[1,0]
	v_pk_mul_f32 v[152:153], v[112:113], s[18:19] op_sel_hi:[1,0]
	v_pk_mul_f32 v[154:155], v[110:111], s[18:19] op_sel_hi:[1,0]
	v_pk_mul_f32 v[156:157], v[108:109], s[18:19] op_sel_hi:[1,0]
	v_pk_mul_f32 v[158:159], v[106:107], s[18:19] op_sel_hi:[1,0]
	v_pk_mul_f32 v[144:145], v[124:125], s[18:19] op_sel_hi:[1,0]
	v_pk_mul_f32 v[146:147], v[122:123], s[18:19] op_sel_hi:[1,0]
	v_pk_mul_f32 v[148:149], v[116:117], s[18:19] op_sel_hi:[1,0]
	v_pk_mul_f32 v[150:151], v[114:115], s[18:19] op_sel_hi:[1,0]
	v_pk_mul_f32 v[132:133], v[104:105], s[18:19] op_sel_hi:[1,0]
	v_pk_mul_f32 v[134:135], v[102:103], s[18:19] op_sel_hi:[1,0]
	v_pk_mul_f32 v[136:137], v[100:101], s[18:19] op_sel_hi:[1,0]
	v_pk_mul_f32 v[138:139], v[98:99], s[18:19] op_sel_hi:[1,0]
	v_pk_mul_f32 v[116:117], v[96:97], s[18:19] op_sel_hi:[1,0]
	v_pk_mul_f32 v[118:119], v[94:95], s[18:19] op_sel_hi:[1,0]
	v_pk_mul_f32 v[120:121], v[92:93], s[18:19] op_sel_hi:[1,0]
	v_pk_mul_f32 v[122:123], v[90:91], s[18:19] op_sel_hi:[1,0]
	v_pk_mul_f32 v[126:127], v[80:81], s[18:19] op_sel_hi:[1,0]
	v_pk_mul_f32 v[124:125], v[78:79], s[18:19] op_sel_hi:[1,0]
	v_pk_mul_f32 v[130:131], v[72:73], s[18:19] op_sel_hi:[1,0]
	v_pk_mul_f32 v[128:129], v[70:71], s[18:19] op_sel_hi:[1,0]
	v_pk_mul_f32 v[108:109], v[88:89], s[18:19] op_sel_hi:[1,0]
	v_pk_mul_f32 v[110:111], v[86:87], s[18:19] op_sel_hi:[1,0]
	v_pk_mul_f32 v[112:113], v[84:85], s[18:19] op_sel_hi:[1,0]
	v_pk_mul_f32 v[114:115], v[82:83], s[18:19] op_sel_hi:[1,0]
	v_pk_mul_f32 v[100:101], v[64:65], s[18:19] op_sel_hi:[1,0]
	v_pk_mul_f32 v[102:103], v[62:63], s[18:19] op_sel_hi:[1,0]
	v_pk_mul_f32 v[104:105], v[56:57], s[18:19] op_sel_hi:[1,0]
	v_pk_mul_f32 v[106:107], v[54:55], s[18:19] op_sel_hi:[1,0]
	v_pk_mul_f32 v[92:93], v[76:77], s[18:19] op_sel_hi:[1,0]
	v_pk_mul_f32 v[94:95], v[74:75], s[18:19] op_sel_hi:[1,0]
	v_pk_mul_f32 v[96:97], v[68:69], s[18:19] op_sel_hi:[1,0]
	v_pk_mul_f32 v[98:99], v[66:67], s[18:19] op_sel_hi:[1,0]
	v_pk_mul_f32 v[84:85], v[48:49], s[18:19] op_sel_hi:[1,0]
	v_pk_mul_f32 v[86:87], v[46:47], s[18:19] op_sel_hi:[1,0]
	v_pk_mul_f32 v[88:89], v[44:45], s[18:19] op_sel_hi:[1,0]
	v_pk_mul_f32 v[90:91], v[42:43], s[18:19] op_sel_hi:[1,0]
	v_pk_mul_f32 v[74:75], v[60:61], s[18:19] op_sel_hi:[1,0]
	v_pk_mul_f32 v[76:77], v[58:59], s[18:19] op_sel_hi:[1,0]
	v_pk_mul_f32 v[78:79], v[52:53], s[18:19] op_sel_hi:[1,0]
	v_pk_mul_f32 v[80:81], v[50:51], s[18:19] op_sel_hi:[1,0]
	v_pk_mul_f32 v[66:67], v[40:41], s[18:19] op_sel_hi:[1,0]
	v_pk_mul_f32 v[68:69], v[38:39], s[18:19] op_sel_hi:[1,0]
	v_pk_mul_f32 v[70:71], v[36:37], s[18:19] op_sel_hi:[1,0]
	v_pk_mul_f32 v[72:73], v[34:35], s[18:19] op_sel_hi:[1,0]

.LBB0_1774:
	s_add_i32 s78, s56, 2
	s_add_u32 s10, s54, 0x80
	s_addc_u32 s11, s55, 0
	s_add_i32 s7, 0, 0x10000
	s_cmp_eq_u32 s64, s56
	s_cselect_b32 s57, s39, s11
	s_cselect_b32 s56, s38, s10
	s_cselect_b32 s59, s53, s77
	s_cselect_b32 s58, s52, s75
	s_add_i32 s10, 0, 0x14000
	v_add_u32_e32 v2, s7, v190
	v_add_u32_e32 v6, s10, v190
	ds_read_b128 v[26:29], v2
	ds_read_b128 v[30:33], v2 offset:1024
	ds_read_b128 v[18:21], v2 offset:2048
	ds_read_b128 v[22:25], v2 offset:3072
	ds_read_b128 v[10:13], v6
	ds_read_b128 v[14:17], v6 offset:1024
	s_waitcnt lgkmcnt(0)
	ds_read_b128 v[2:5], v6 offset:2048
	ds_read_b128 v[6:9], v6 offset:3072
	v_lshl_add_u64 v[200:201], s[54:55], 0, v[168:169]
	s_add_i32 m0, s16, 0xc000
	ds_read_b128 v[172:175], v191
	ds_read_b128 v[176:179], v191 offset:1024
	ds_read_b128 v[180:183], v191 offset:2048
	ds_read_b128 v[184:187], v191 offset:3072
	ds_read_b128 v[192:195], v191 offset:4096
	ds_read_b128 v[196:199], v191 offset:5120
	ds_read_b128 v[210:213], v191 offset:6144
	ds_read_b128 v[214:217], v191 offset:7168
	global_load_lds_dwordx4 v[200:201], off
	v_lshl_add_u64 v[200:201], s[54:55], 0, v[170:171]
	s_add_i32 m0, s16, 0xe000
	s_nop 0
	global_load_lds_dwordx4 v[200:201], off
	s_waitcnt vmcnt(8)
	s_waitcnt lgkmcnt(0)
	s_setprio 1
	s_barrier
	v_mfma_f32_16x16x128_f8f6f4 v[158:161], v[26:33], v[172:179], v[158:161]
	v_mfma_f32_16x16x128_f8f6f4 v[154:157], v[18:25], v[172:179], v[154:157]
	v_mfma_f32_16x16x128_f8f6f4 v[150:153], v[26:33], v[180:187], v[150:153]
	v_mfma_f32_16x16x128_f8f6f4 v[146:149], v[18:25], v[180:187], v[146:149]
	v_mfma_f32_16x16x128_f8f6f4 v[138:141], v[26:33], v[192:199], v[138:141]
	v_mfma_f32_16x16x128_f8f6f4 v[130:133], v[18:25], v[192:199], v[130:133]
	v_mfma_f32_16x16x128_f8f6f4 v[122:125], v[26:33], v[210:217], v[122:125]
	v_mfma_f32_16x16x128_f8f6f4 v[114:117], v[18:25], v[210:217], v[114:117]
	v_mfma_f32_16x16x128_f8f6f4 v[142:145], v[10:17], v[172:179], v[142:145]
	v_mfma_f32_16x16x128_f8f6f4 v[134:137], v[2:9], v[172:179], v[134:137]
	v_mfma_f32_16x16x128_f8f6f4 v[126:129], v[10:17], v[180:187], v[126:129]
	v_mfma_f32_16x16x128_f8f6f4 v[118:121], v[2:9], v[180:187], v[118:121]
	v_mfma_f32_16x16x128_f8f6f4 v[110:113], v[10:17], v[192:199], v[110:113]
	v_mfma_f32_16x16x128_f8f6f4 v[106:109], v[2:9], v[192:199], v[106:109]
	v_mfma_f32_16x16x128_f8f6f4 v[102:105], v[10:17], v[210:217], v[102:105]
	v_mfma_f32_16x16x128_f8f6f4 v[98:101], v[2:9], v[210:217], v[98:101]
	s_setprio 0
	s_barrier
	s_add_i32 s7, s7, s13
	v_lshl_add_u64 v[172:173], s[58:59], 0, v[0:1]
	s_mov_b32 m0, s7
	ds_read_b128 v[192:195], v191 offset:16384
	ds_read_b128 v[196:199], v191 offset:17408
	ds_read_b128 v[210:213], v191 offset:18432
	ds_read_b128 v[214:217], v191 offset:19456
	ds_read_b128 v[218:221], v191 offset:20480
	ds_read_b128 v[222:225], v191 offset:21504
	ds_read_b128 v[246:249], v191 offset:22528
	ds_read_b128 v[250:253], v191 offset:23552
	global_load_lds_dwordx4 v[172:173], off
	s_add_i32 m0, s7, 0x2000
	v_lshl_add_u64 v[174:175], s[58:59], 0, v[166:167]
	s_add_u32 s58, s58, s28
	s_addc_u32 s59, s59, s29
	s_add_i32 s7, s10, s13
	global_load_lds_dwordx4 v[174:175], off
	v_lshl_add_u64 v[176:177], s[58:59], 0, v[0:1]
	s_mov_b32 m0, s7
	v_lshl_add_u64 v[178:179], s[58:59], 0, v[166:167]
	global_load_lds_dwordx4 v[176:177], off
	s_add_i32 m0, s7, 0x2000
	v_lshl_add_u64 v[180:181], s[56:57], 0, v[162:163]
	global_load_lds_dwordx4 v[178:179], off
	s_mov_b32 m0, s16
	v_lshl_add_u64 v[182:183], s[56:57], 0, v[164:165]
	global_load_lds_dwordx4 v[180:181], off
	s_mov_b32 m0, s17
	s_nop 0
	global_load_lds_dwordx4 v[182:183], off
	s_waitcnt vmcnt(8)
	s_waitcnt lgkmcnt(0)
	s_setprio 1
	s_barrier
	v_mfma_f32_16x16x128_f8f6f4 v[94:97], v[26:33], v[192:199], v[94:97]
	v_mfma_f32_16x16x128_f8f6f4 v[90:93], v[18:25], v[192:199], v[90:93]
	v_mfma_f32_16x16x128_f8f6f4 v[86:89], v[26:33], v[210:217], v[86:89]
	v_mfma_f32_16x16x128_f8f6f4 v[82:85], v[18:25], v[210:217], v[82:85]
	v_mfma_f32_16x16x128_f8f6f4 v[74:77], v[26:33], v[218:225], v[74:77]
	v_mfma_f32_16x16x128_f8f6f4 v[66:69], v[18:25], v[218:225], v[66:69]
	v_mfma_f32_16x16x128_f8f6f4 v[58:61], v[26:33], v[246:253], v[58:61]
	v_mfma_f32_16x16x128_f8f6f4 v[50:53], v[18:25], v[246:253], v[50:53]
	v_mfma_f32_16x16x128_f8f6f4 v[78:81], v[10:17], v[192:199], v[78:81]
	v_mfma_f32_16x16x128_f8f6f4 v[70:73], v[2:9], v[192:199], v[70:73]
	v_mfma_f32_16x16x128_f8f6f4 v[62:65], v[10:17], v[210:217], v[62:65]
	v_mfma_f32_16x16x128_f8f6f4 v[54:57], v[2:9], v[210:217], v[54:57]
	v_mfma_f32_16x16x128_f8f6f4 v[46:49], v[10:17], v[218:225], v[46:49]
	v_mfma_f32_16x16x128_f8f6f4 v[42:45], v[2:9], v[218:225], v[42:45]
	v_mfma_f32_16x16x128_f8f6f4 v[38:41], v[10:17], v[246:253], v[38:41]
	v_mfma_f32_16x16x128_f8f6f4 v[34:37], v[2:9], v[246:253], v[34:37]
	s_setprio 0
	s_barrier
	s_add_i32 s7, 0, 0x18000
	s_add_i32 s58, 0, 0x1c000
	v_add_u32_e32 v14, s7, v190
	v_add_u32_e32 v30, s58, v190
	ds_read_b128 v[2:5], v14
	ds_read_b128 v[6:9], v14 offset:1024
	ds_read_b128 v[10:13], v14 offset:2048
	ds_read_b128 v[14:17], v14 offset:3072
	ds_read_b128 v[18:21], v30
	ds_read_b128 v[22:25], v30 offset:1024
	ds_read_b128 v[26:29], v30 offset:2048
	ds_read_b128 v[30:33], v30 offset:3072
	s_add_u32 s10, s56, s28
	s_addc_u32 s11, s57, s29
	s_mov_b32 m0, s23
	v_lshl_add_u64 v[184:185], s[10:11], 0, v[162:163]
	ds_read_b128 v[192:195], v191 offset:32768
	ds_read_b128 v[196:199], v191 offset:33792
	ds_read_b128 v[210:213], v191 offset:34816
	ds_read_b128 v[214:217], v191 offset:35840
	ds_read_b128 v[218:221], v191 offset:36864
	ds_read_b128 v[222:225], v191 offset:37888
	ds_read_b128 v[246:249], v191 offset:38912
	ds_read_b128 v[250:253], v191 offset:39936
	global_load_lds_dwordx4 v[184:185], off
	v_lshl_add_u64 v[184:185], s[10:11], 0, v[164:165]
	s_mov_b32 m0, s26
	s_nop 0
	global_load_lds_dwordx4 v[184:185], off
	s_waitcnt vmcnt(8)
	s_waitcnt lgkmcnt(0)
	s_setprio 1
	s_barrier
	v_mfma_f32_16x16x128_f8f6f4 v[158:161], v[2:9], v[192:199], v[158:161]
	v_mfma_f32_16x16x128_f8f6f4 v[154:157], v[10:17], v[192:199], v[154:157]
	v_mfma_f32_16x16x128_f8f6f4 v[150:153], v[2:9], v[210:217], v[150:153]
	v_mfma_f32_16x16x128_f8f6f4 v[146:149], v[10:17], v[210:217], v[146:149]
	v_mfma_f32_16x16x128_f8f6f4 v[138:141], v[2:9], v[218:225], v[138:141]
	v_mfma_f32_16x16x128_f8f6f4 v[130:133], v[10:17], v[218:225], v[130:133]
	v_mfma_f32_16x16x128_f8f6f4 v[122:125], v[2:9], v[246:253], v[122:125]
	v_mfma_f32_16x16x128_f8f6f4 v[114:117], v[10:17], v[246:253], v[114:117]
	v_mfma_f32_16x16x128_f8f6f4 v[142:145], v[18:25], v[192:199], v[142:145]
	v_mfma_f32_16x16x128_f8f6f4 v[134:137], v[26:33], v[192:199], v[134:137]
	v_mfma_f32_16x16x128_f8f6f4 v[126:129], v[18:25], v[210:217], v[126:129]
	v_mfma_f32_16x16x128_f8f6f4 v[118:121], v[26:33], v[210:217], v[118:121]
	v_mfma_f32_16x16x128_f8f6f4 v[110:113], v[18:25], v[218:225], v[110:113]
	v_mfma_f32_16x16x128_f8f6f4 v[106:109], v[26:33], v[218:225], v[106:109]
	v_mfma_f32_16x16x128_f8f6f4 v[102:105], v[18:25], v[246:253], v[102:105]
	v_mfma_f32_16x16x128_f8f6f4 v[98:101], v[26:33], v[246:253], v[98:101]
	s_setprio 0
	s_barrier
	s_add_i32 s7, s7, s13
	v_lshl_add_u64 v[172:173], v[172:173], 0, s[14:15]
	s_mov_b32 m0, s7
	ds_read_b128 v[192:195], v191 offset:49152
	ds_read_b128 v[196:199], v191 offset:50176
	ds_read_b128 v[210:213], v191 offset:51200
	ds_read_b128 v[214:217], v191 offset:52224
	ds_read_b128 v[218:221], v191 offset:53248
	ds_read_b128 v[222:225], v191 offset:54272
	ds_read_b128 v[246:249], v191 offset:55296
	ds_read_b128 v[250:253], v191 offset:56320
	global_load_lds_dwordx4 v[172:173], off
	v_lshl_add_u64 v[172:173], v[174:175], 0, s[14:15]
	s_add_i32 m0, s7, 0x2000
	s_add_i32 s7, s58, s13
	global_load_lds_dwordx4 v[172:173], off
	v_lshl_add_u64 v[172:173], v[176:177], 0, s[14:15]
	s_mov_b32 m0, s7
	s_nop 0
	global_load_lds_dwordx4 v[172:173], off
	v_lshl_add_u64 v[172:173], v[178:179], 0, s[14:15]
	s_add_i32 m0, s7, 0x2000
	s_nop 0
	global_load_lds_dwordx4 v[172:173], off
	v_lshl_add_u64 v[172:173], v[180:181], 0, s[14:15]
	s_mov_b32 m0, s27
	s_nop 0
	global_load_lds_dwordx4 v[172:173], off
	v_lshl_add_u64 v[172:173], v[182:183], 0, s[14:15]
	s_mov_b32 m0, s60
	s_nop 0
	global_load_lds_dwordx4 v[172:173], off
	s_waitcnt vmcnt(8)
	s_waitcnt lgkmcnt(0)
	s_setprio 1
	s_barrier
	v_mfma_f32_16x16x128_f8f6f4 v[94:97], v[2:9], v[192:199], v[94:97]
	v_mfma_f32_16x16x128_f8f6f4 v[90:93], v[10:17], v[192:199], v[90:93]
	v_mfma_f32_16x16x128_f8f6f4 v[86:89], v[2:9], v[210:217], v[86:89]
	v_mfma_f32_16x16x128_f8f6f4 v[82:85], v[10:17], v[210:217], v[82:85]
	v_mfma_f32_16x16x128_f8f6f4 v[74:77], v[2:9], v[218:225], v[74:77]
	v_mfma_f32_16x16x128_f8f6f4 v[66:69], v[10:17], v[218:225], v[66:69]
	v_mfma_f32_16x16x128_f8f6f4 v[58:61], v[2:9], v[246:253], v[58:61]
	v_mfma_f32_16x16x128_f8f6f4 v[50:53], v[10:17], v[246:253], v[50:53]
	v_mfma_f32_16x16x128_f8f6f4 v[78:81], v[18:25], v[192:199], v[78:81]
	v_mfma_f32_16x16x128_f8f6f4 v[70:73], v[26:33], v[192:199], v[70:73]
	v_mfma_f32_16x16x128_f8f6f4 v[62:65], v[18:25], v[210:217], v[62:65]
	v_mfma_f32_16x16x128_f8f6f4 v[54:57], v[26:33], v[210:217], v[54:57]
	v_mfma_f32_16x16x128_f8f6f4 v[46:49], v[18:25], v[218:225], v[46:49]
	v_mfma_f32_16x16x128_f8f6f4 v[42:45], v[26:33], v[218:225], v[42:45]
	v_mfma_f32_16x16x128_f8f6f4 v[38:41], v[18:25], v[246:253], v[38:41]
	v_mfma_f32_16x16x128_f8f6f4 v[34:37], v[26:33], v[246:253], v[34:37]
	s_setprio 0
	s_barrier
	s_add_u32 s54, s54, 0x100
	s_addc_u32 s55, s55, 0
	s_add_u32 s75, s75, 0x100
	s_addc_u32 s77, s77, 0
	s_cmp_ge_i32 s78, s61
	s_mov_b32 s56, s78
	s_cbranch_scc0 .LBB0_1774
	v_pk_mul_f32 v[160:161], v[160:161], s[18:19] op_sel_hi:[1,0]
	v_pk_mul_f32 v[158:159], v[158:159], s[18:19] op_sel_hi:[1,0]
	v_pk_mul_f32 v[172:173], v[156:157], s[18:19] op_sel_hi:[1,0]
	v_pk_mul_f32 v[174:175], v[154:155], s[18:19] op_sel_hi:[1,0]
	v_pk_mul_f32 v[176:177], v[144:145], s[18:19] op_sel_hi:[1,0]
	v_pk_mul_f32 v[178:179], v[142:143], s[18:19] op_sel_hi:[1,0]
	v_pk_mul_f32 v[180:181], v[136:137], s[18:19] op_sel_hi:[1,0]
	v_pk_mul_f32 v[182:183], v[134:135], s[18:19] op_sel_hi:[1,0]
	v_pk_mul_f32 v[156:157], v[152:153], s[18:19] op_sel_hi:[1,0]
	v_pk_mul_f32 v[154:155], v[150:151], s[18:19] op_sel_hi:[1,0]
	v_pk_mul_f32 v[152:153], v[148:149], s[18:19] op_sel_hi:[1,0]
	v_pk_mul_f32 v[150:151], v[146:147], s[18:19] op_sel_hi:[1,0]
	v_pk_mul_f32 v[148:149], v[128:129], s[18:19] op_sel_hi:[1,0]
	v_pk_mul_f32 v[146:147], v[126:127], s[18:19] op_sel_hi:[1,0]
	v_pk_mul_f32 v[144:145], v[120:121], s[18:19] op_sel_hi:[1,0]
	v_pk_mul_f32 v[142:143], v[118:119], s[18:19] op_sel_hi:[1,0]
	v_pk_mul_f32 v[126:127], v[140:141], s[18:19] op_sel_hi:[1,0]
	v_pk_mul_f32 v[128:129], v[138:139], s[18:19] op_sel_hi:[1,0]
	v_pk_mul_f32 v[132:133], v[132:133], s[18:19] op_sel_hi:[1,0]
	v_pk_mul_f32 v[130:131], v[130:131], s[18:19] op_sel_hi:[1,0]
	v_pk_mul_f32 v[134:135], v[112:113], s[18:19] op_sel_hi:[1,0]
	v_pk_mul_f32 v[136:137], v[110:111], s[18:19] op_sel_hi:[1,0]
	v_pk_mul_f32 v[138:139], v[108:109], s[18:19] op_sel_hi:[1,0]
	v_pk_mul_f32 v[140:141], v[106:107], s[18:19] op_sel_hi:[1,0]
	v_pk_mul_f32 v[120:121], v[124:125], s[18:19] op_sel_hi:[1,0]
	v_pk_mul_f32 v[118:119], v[122:123], s[18:19] op_sel_hi:[1,0]
	v_pk_mul_f32 v[116:117], v[116:117], s[18:19] op_sel_hi:[1,0]
	v_pk_mul_f32 v[114:115], v[114:115], s[18:19] op_sel_hi:[1,0]
	v_pk_mul_f32 v[112:113], v[104:105], s[18:19] op_sel_hi:[1,0]
	v_pk_mul_f32 v[110:111], v[102:103], s[18:19] op_sel_hi:[1,0]
	v_pk_mul_f32 v[108:109], v[100:101], s[18:19] op_sel_hi:[1,0]
	v_pk_mul_f32 v[106:107], v[98:99], s[18:19] op_sel_hi:[1,0]
	v_pk_mul_f32 v[96:97], v[96:97], s[18:19] op_sel_hi:[1,0]
	v_pk_mul_f32 v[94:95], v[94:95], s[18:19] op_sel_hi:[1,0]
	v_pk_mul_f32 v[92:93], v[92:93], s[18:19] op_sel_hi:[1,0]
	v_pk_mul_f32 v[90:91], v[90:91], s[18:19] op_sel_hi:[1,0]
	v_pk_mul_f32 v[98:99], v[80:81], s[18:19] op_sel_hi:[1,0]
	v_pk_mul_f32 v[100:101], v[78:79], s[18:19] op_sel_hi:[1,0]
	v_pk_mul_f32 v[102:103], v[72:73], s[18:19] op_sel_hi:[1,0]
	v_pk_mul_f32 v[104:105], v[70:71], s[18:19] op_sel_hi:[1,0]
	v_pk_mul_f32 v[88:89], v[88:89], s[18:19] op_sel_hi:[1,0]
	v_pk_mul_f32 v[86:87], v[86:87], s[18:19] op_sel_hi:[1,0]
	v_pk_mul_f32 v[84:85], v[84:85], s[18:19] op_sel_hi:[1,0]
	v_pk_mul_f32 v[82:83], v[82:83], s[18:19] op_sel_hi:[1,0]
	v_pk_mul_f32 v[80:81], v[64:65], s[18:19] op_sel_hi:[1,0]
	v_pk_mul_f32 v[78:79], v[62:63], s[18:19] op_sel_hi:[1,0]
	v_pk_mul_f32 v[72:73], v[56:57], s[18:19] op_sel_hi:[1,0]
	v_pk_mul_f32 v[70:71], v[54:55], s[18:19] op_sel_hi:[1,0]
	v_pk_mul_f32 v[54:55], v[76:77], s[18:19] op_sel_hi:[1,0]
	v_pk_mul_f32 v[56:57], v[74:75], s[18:19] op_sel_hi:[1,0]
	v_pk_mul_f32 v[62:63], v[68:69], s[18:19] op_sel_hi:[1,0]
	v_pk_mul_f32 v[64:65], v[66:67], s[18:19] op_sel_hi:[1,0]
	v_pk_mul_f32 v[48:49], v[48:49], s[18:19] op_sel_hi:[1,0]
	v_pk_mul_f32 v[46:47], v[46:47], s[18:19] op_sel_hi:[1,0]
	v_pk_mul_f32 v[44:45], v[44:45], s[18:19] op_sel_hi:[1,0]
	v_pk_mul_f32 v[42:43], v[42:43], s[18:19] op_sel_hi:[1,0]
	v_pk_mul_f32 v[32:33], v[60:61], s[18:19] op_sel_hi:[1,0]
	v_pk_mul_f32 v[30:31], v[58:59], s[18:19] op_sel_hi:[1,0]
	v_pk_mul_f32 v[28:29], v[52:53], s[18:19] op_sel_hi:[1,0]
	v_pk_mul_f32 v[26:27], v[50:51], s[18:19] op_sel_hi:[1,0]
	v_pk_mul_f32 v[24:25], v[40:41], s[18:19] op_sel_hi:[1,0]
	v_pk_mul_f32 v[22:23], v[38:39], s[18:19] op_sel_hi:[1,0]
	v_pk_mul_f32 v[20:21], v[36:37], s[18:19] op_sel_hi:[1,0]
	v_pk_mul_f32 v[18:19], v[34:35], s[18:19] op_sel_hi:[1,0]

.LBB0_1873:
	s_add_i32 s69, s54, 2
	s_add_u32 s7, s52, 0x80
	s_addc_u32 s10, s53, 0
	s_add_i32 s70, 0, 0x10000
	s_cmp_eq_u32 s61, s54
	s_cselect_b32 s55, s39, s10
	s_cselect_b32 s54, s38, s7
	s_cselect_b32 s11, s51, s68
	s_cselect_b32 s10, s50, s67
	s_add_i32 s7, 0, 0x14000
	v_add_u32_e32 v46, s70, v178
	v_add_u32_e32 v62, s7, v178
	ds_read_b128 v[34:37], v46
	ds_read_b128 v[38:41], v46 offset:1024
	ds_read_b128 v[42:45], v46 offset:2048
	ds_read_b128 v[46:49], v46 offset:3072
	ds_read_b128 v[50:53], v62
	ds_read_b128 v[54:57], v62 offset:1024
	ds_read_b128 v[58:61], v62 offset:2048
	ds_read_b128 v[62:65], v62 offset:3072
	v_lshl_add_u64 v[200:201], s[52:53], 0, v[168:169]
	s_add_i32 m0, s23, 0xc000
	ds_read_b128 v[172:175], v179
	ds_read_b128 v[180:183], v179 offset:1024
	ds_read_b128 v[184:187], v179 offset:2048
	ds_read_b128 v[188:191], v179 offset:3072
	ds_read_b128 v[192:195], v179 offset:4096
	ds_read_b128 v[196:199], v179 offset:5120
	ds_read_b128 v[210:213], v179 offset:6144
	ds_read_b128 v[214:217], v179 offset:7168
	global_load_lds_dwordx4 v[200:201], off
	v_lshl_add_u64 v[200:201], s[52:53], 0, v[170:171]
	s_add_i32 m0, s23, 0xe000
	s_nop 0
	global_load_lds_dwordx4 v[200:201], off
	s_waitcnt vmcnt(8)
	s_waitcnt lgkmcnt(0)
	s_setprio 1
	s_barrier
	v_mfma_f32_16x16x32_bf16 v[158:161], v[34:37], v[172:175], v[158:161]
	v_mfma_f32_16x16x32_bf16 v[154:157], v[42:45], v[172:175], v[154:157]
	v_mfma_f32_16x16x32_bf16 v[142:145], v[34:37], v[184:187], v[142:145]
	v_mfma_f32_16x16x32_bf16 v[138:141], v[42:45], v[184:187], v[138:141]
	v_mfma_f32_16x16x32_bf16 v[126:129], v[34:37], v[192:195], v[126:129]
	v_mfma_f32_16x16x32_bf16 v[122:125], v[42:45], v[192:195], v[122:125]
	v_mfma_f32_16x16x32_bf16 v[110:113], v[34:37], v[210:213], v[110:113]
	v_mfma_f32_16x16x32_bf16 v[106:109], v[42:45], v[210:213], v[106:109]
	v_mfma_f32_16x16x32_bf16 v[158:161], v[38:41], v[180:183], v[158:161]
	v_mfma_f32_16x16x32_bf16 v[154:157], v[46:49], v[180:183], v[154:157]
	v_mfma_f32_16x16x32_bf16 v[142:145], v[38:41], v[188:191], v[142:145]
	v_mfma_f32_16x16x32_bf16 v[138:141], v[46:49], v[188:191], v[138:141]
	v_mfma_f32_16x16x32_bf16 v[126:129], v[38:41], v[196:199], v[126:129]
	v_mfma_f32_16x16x32_bf16 v[122:125], v[46:49], v[196:199], v[122:125]
	v_mfma_f32_16x16x32_bf16 v[110:113], v[38:41], v[214:217], v[110:113]
	v_mfma_f32_16x16x32_bf16 v[106:109], v[46:49], v[214:217], v[106:109]
	v_mfma_f32_16x16x32_bf16 v[150:153], v[50:53], v[172:175], v[150:153]
	v_mfma_f32_16x16x32_bf16 v[146:149], v[58:61], v[172:175], v[146:149]
	v_mfma_f32_16x16x32_bf16 v[134:137], v[50:53], v[184:187], v[134:137]
	v_mfma_f32_16x16x32_bf16 v[130:133], v[58:61], v[184:187], v[130:133]
	v_mfma_f32_16x16x32_bf16 v[118:121], v[50:53], v[192:195], v[118:121]
	v_mfma_f32_16x16x32_bf16 v[114:117], v[58:61], v[192:195], v[114:117]
	v_mfma_f32_16x16x32_bf16 v[102:105], v[50:53], v[210:213], v[102:105]
	v_mfma_f32_16x16x32_bf16 v[98:101], v[58:61], v[210:213], v[98:101]
	v_mfma_f32_16x16x32_bf16 v[150:153], v[54:57], v[180:183], v[150:153]
	v_mfma_f32_16x16x32_bf16 v[146:149], v[62:65], v[180:183], v[146:149]
	v_mfma_f32_16x16x32_bf16 v[134:137], v[54:57], v[188:191], v[134:137]
	v_mfma_f32_16x16x32_bf16 v[130:133], v[62:65], v[188:191], v[130:133]
	v_mfma_f32_16x16x32_bf16 v[118:121], v[54:57], v[196:199], v[118:121]
	v_mfma_f32_16x16x32_bf16 v[114:117], v[62:65], v[196:199], v[114:117]
	v_mfma_f32_16x16x32_bf16 v[102:105], v[54:57], v[214:217], v[102:105]
	v_mfma_f32_16x16x32_bf16 v[98:101], v[62:65], v[214:217], v[98:101]
	s_setprio 0
	s_barrier
	s_add_i32 s70, s70, s17
	v_lshl_add_u64 v[200:201], s[10:11], 0, v[0:1]
	s_mov_b32 m0, s70
	ds_read_b128 v[172:175], v179 offset:16384
	ds_read_b128 v[180:183], v179 offset:17408
	ds_read_b128 v[184:187], v179 offset:18432
	ds_read_b128 v[188:191], v179 offset:19456
	ds_read_b128 v[192:195], v179 offset:20480
	ds_read_b128 v[196:199], v179 offset:21504
	ds_read_b128 v[210:213], v179 offset:22528
	ds_read_b128 v[214:217], v179 offset:23552
	global_load_lds_dwordx4 v[200:201], off
	s_add_i32 m0, s70, 0x2000
	v_lshl_add_u64 v[202:203], s[10:11], 0, v[166:167]
	s_add_u32 s10, s10, s0
	s_addc_u32 s11, s11, s1
	s_add_i32 s7, s7, s17
	global_load_lds_dwordx4 v[202:203], off
	v_lshl_add_u64 v[226:227], s[10:11], 0, v[0:1]
	s_mov_b32 m0, s7
	v_lshl_add_u64 v[228:229], s[10:11], 0, v[166:167]
	global_load_lds_dwordx4 v[226:227], off
	s_add_i32 m0, s7, 0x2000
	v_lshl_add_u64 v[230:231], s[54:55], 0, v[162:163]
	global_load_lds_dwordx4 v[228:229], off
	s_mov_b32 m0, s23
	v_lshl_add_u64 v[232:233], s[54:55], 0, v[164:165]
	global_load_lds_dwordx4 v[230:231], off
	s_mov_b32 m0, s26
	s_nop 0
	global_load_lds_dwordx4 v[232:233], off
	s_waitcnt vmcnt(8)
	s_waitcnt lgkmcnt(0)
	s_setprio 1
	s_barrier
	v_mfma_f32_16x16x32_bf16 v[94:97], v[34:37], v[172:175], v[94:97]
	v_mfma_f32_16x16x32_bf16 v[90:93], v[42:45], v[172:175], v[90:93]
	v_mfma_f32_16x16x32_bf16 v[78:81], v[34:37], v[184:187], v[78:81]
	v_mfma_f32_16x16x32_bf16 v[74:77], v[42:45], v[184:187], v[74:77]
	v_mfma_f32_16x16x32_bf16 v[30:33], v[34:37], v[192:195], v[30:33]
	v_mfma_f32_16x16x32_bf16 v[26:29], v[42:45], v[192:195], v[26:29]
	v_mfma_f32_16x16x32_bf16 v[14:17], v[34:37], v[210:213], v[14:17]
	v_mfma_f32_16x16x32_bf16 v[10:13], v[42:45], v[210:213], v[10:13]
	v_mfma_f32_16x16x32_bf16 v[94:97], v[38:41], v[180:183], v[94:97]
	v_mfma_f32_16x16x32_bf16 v[90:93], v[46:49], v[180:183], v[90:93]
	v_mfma_f32_16x16x32_bf16 v[78:81], v[38:41], v[188:191], v[78:81]
	v_mfma_f32_16x16x32_bf16 v[74:77], v[46:49], v[188:191], v[74:77]
	v_mfma_f32_16x16x32_bf16 v[30:33], v[38:41], v[196:199], v[30:33]
	v_mfma_f32_16x16x32_bf16 v[26:29], v[46:49], v[196:199], v[26:29]
	v_mfma_f32_16x16x32_bf16 v[14:17], v[38:41], v[214:217], v[14:17]
	v_mfma_f32_16x16x32_bf16 v[10:13], v[46:49], v[214:217], v[10:13]
	v_mfma_f32_16x16x32_bf16 v[22:25], v[50:53], v[192:195], v[22:25]
	v_mfma_f32_16x16x32_bf16 v[18:21], v[58:61], v[192:195], v[18:21]
	v_mfma_f32_16x16x32_bf16 v[6:9], v[50:53], v[210:213], v[6:9]
	v_mfma_f32_16x16x32_bf16 v[2:5], v[58:61], v[210:213], v[2:5]
	v_mfma_f32_16x16x32_bf16 v[34:37], v[50:53], v[172:175], v[86:89]
	v_mfma_f32_16x16x32_bf16 v[38:41], v[58:61], v[172:175], v[82:85]
	v_mfma_f32_16x16x32_bf16 v[42:45], v[50:53], v[184:187], v[70:73]
	v_mfma_f32_16x16x32_bf16 v[46:49], v[58:61], v[184:187], v[66:69]
	v_mfma_f32_16x16x32_bf16 v[22:25], v[54:57], v[196:199], v[22:25]
	v_mfma_f32_16x16x32_bf16 v[18:21], v[62:65], v[196:199], v[18:21]
	v_mfma_f32_16x16x32_bf16 v[6:9], v[54:57], v[214:217], v[6:9]
	v_mfma_f32_16x16x32_bf16 v[2:5], v[62:65], v[214:217], v[2:5]
	v_mfma_f32_16x16x32_bf16 v[34:37], v[54:57], v[180:183], v[34:37]
	v_mfma_f32_16x16x32_bf16 v[38:41], v[62:65], v[180:183], v[38:41]
	v_mfma_f32_16x16x32_bf16 v[42:45], v[54:57], v[188:191], v[42:45]
	v_mfma_f32_16x16x32_bf16 v[46:49], v[62:65], v[188:191], v[46:49]
	s_setprio 0
	s_barrier
	s_add_i32 s7, 0, 0x18000
	s_add_i32 s70, 0, 0x1c000
	v_add_u32_e32 v62, s7, v178
	v_add_u32_e32 v66, s70, v178
	ds_read_b128 v[50:53], v62
	ds_read_b128 v[54:57], v62 offset:1024
	ds_read_b128 v[58:61], v62 offset:2048
	ds_read_b128 v[62:65], v62 offset:3072
	ds_read_b128 v[172:175], v66
	ds_read_b128 v[180:183], v66 offset:1024
	ds_read_b128 v[184:187], v66 offset:2048
	ds_read_b128 v[188:191], v66 offset:3072
	s_add_u32 s10, s54, s0
	s_addc_u32 s11, s55, s1
	s_mov_b32 m0, s27
	v_lshl_add_u64 v[218:219], s[10:11], 0, v[162:163]
	ds_read_b128 v[66:69], v179 offset:32768
	ds_read_b128 v[70:73], v179 offset:33792
	ds_read_b128 v[82:85], v179 offset:34816
	ds_read_b128 v[86:89], v179 offset:35840
	ds_read_b128 v[192:195], v179 offset:36864
	ds_read_b128 v[196:199], v179 offset:37888
	ds_read_b128 v[210:213], v179 offset:38912
	ds_read_b128 v[214:217], v179 offset:39936
	global_load_lds_dwordx4 v[218:219], off
	v_lshl_add_u64 v[218:219], s[10:11], 0, v[164:165]
	s_mov_b32 m0, s56
	s_nop 0
	global_load_lds_dwordx4 v[218:219], off
	s_waitcnt vmcnt(8)
	s_waitcnt lgkmcnt(0)
	s_setprio 1
	s_barrier
	v_mfma_f32_16x16x32_bf16 v[158:161], v[50:53], v[66:69], v[158:161]
	v_mfma_f32_16x16x32_bf16 v[154:157], v[58:61], v[66:69], v[154:157]
	v_mfma_f32_16x16x32_bf16 v[142:145], v[50:53], v[82:85], v[142:145]
	v_mfma_f32_16x16x32_bf16 v[138:141], v[58:61], v[82:85], v[138:141]
	v_mfma_f32_16x16x32_bf16 v[126:129], v[50:53], v[192:195], v[126:129]
	v_mfma_f32_16x16x32_bf16 v[122:125], v[58:61], v[192:195], v[122:125]
	v_mfma_f32_16x16x32_bf16 v[110:113], v[50:53], v[210:213], v[110:113]
	v_mfma_f32_16x16x32_bf16 v[106:109], v[58:61], v[210:213], v[106:109]
	v_mfma_f32_16x16x32_bf16 v[158:161], v[54:57], v[70:73], v[158:161]
	v_mfma_f32_16x16x32_bf16 v[154:157], v[62:65], v[70:73], v[154:157]
	v_mfma_f32_16x16x32_bf16 v[142:145], v[54:57], v[86:89], v[142:145]
	v_mfma_f32_16x16x32_bf16 v[138:141], v[62:65], v[86:89], v[138:141]
	v_mfma_f32_16x16x32_bf16 v[126:129], v[54:57], v[196:199], v[126:129]
	v_mfma_f32_16x16x32_bf16 v[122:125], v[62:65], v[196:199], v[122:125]
	v_mfma_f32_16x16x32_bf16 v[110:113], v[54:57], v[214:217], v[110:113]
	v_mfma_f32_16x16x32_bf16 v[106:109], v[62:65], v[214:217], v[106:109]
	v_mfma_f32_16x16x32_bf16 v[150:153], v[172:175], v[66:69], v[150:153]
	v_mfma_f32_16x16x32_bf16 v[66:69], v[184:187], v[66:69], v[146:149]
	v_mfma_f32_16x16x32_bf16 v[146:149], v[188:191], v[70:73], v[66:69]
	v_mfma_f32_16x16x32_bf16 v[66:69], v[172:175], v[82:85], v[134:137]
	v_mfma_f32_16x16x32_bf16 v[134:137], v[180:183], v[86:89], v[66:69]
	v_mfma_f32_16x16x32_bf16 v[66:69], v[184:187], v[82:85], v[130:133]
	v_mfma_f32_16x16x32_bf16 v[130:133], v[188:191], v[86:89], v[66:69]
	v_mfma_f32_16x16x32_bf16 v[66:69], v[172:175], v[192:195], v[118:121]
	v_mfma_f32_16x16x32_bf16 v[118:121], v[180:183], v[196:199], v[66:69]
	v_mfma_f32_16x16x32_bf16 v[66:69], v[184:187], v[192:195], v[114:117]
	v_mfma_f32_16x16x32_bf16 v[114:117], v[188:191], v[196:199], v[66:69]
	v_mfma_f32_16x16x32_bf16 v[66:69], v[172:175], v[210:213], v[102:105]
	v_mfma_f32_16x16x32_bf16 v[102:105], v[180:183], v[214:217], v[66:69]
	v_mfma_f32_16x16x32_bf16 v[66:69], v[184:187], v[210:213], v[98:101]
	v_mfma_f32_16x16x32_bf16 v[150:153], v[180:183], v[70:73], v[150:153]
	v_mfma_f32_16x16x32_bf16 v[98:101], v[188:191], v[214:217], v[66:69]
	s_setprio 0
	s_barrier
	s_add_i32 s7, s7, s17
	v_lshl_add_u64 v[82:83], v[200:201], 0, s[14:15]
	s_mov_b32 m0, s7
	s_nop 0
	ds_read_b128 v[66:69], v179 offset:49152
	ds_read_b128 v[70:73], v179 offset:50176
	ds_read_b128 v[192:195], v179 offset:51200
	ds_read_b128 v[196:199], v179 offset:52224
	ds_read_b128 v[210:213], v179 offset:53248
	ds_read_b128 v[214:217], v179 offset:54272
	ds_read_b128 v[218:221], v179 offset:55296
	ds_read_b128 v[222:225], v179 offset:56320
	global_load_lds_dwordx4 v[82:83], off
	v_lshl_add_u64 v[82:83], v[202:203], 0, s[14:15]
	s_add_i32 m0, s7, 0x2000
	s_add_i32 s7, s70, s17
	global_load_lds_dwordx4 v[82:83], off
	v_lshl_add_u64 v[82:83], v[226:227], 0, s[14:15]
	s_mov_b32 m0, s7
	s_nop 0
	global_load_lds_dwordx4 v[82:83], off
	v_lshl_add_u64 v[82:83], v[228:229], 0, s[14:15]
	s_add_i32 m0, s7, 0x2000
	s_nop 0
	global_load_lds_dwordx4 v[82:83], off
	v_lshl_add_u64 v[82:83], v[230:231], 0, s[14:15]
	s_mov_b32 m0, s8
	s_nop 0
	global_load_lds_dwordx4 v[82:83], off
	v_lshl_add_u64 v[82:83], v[232:233], 0, s[14:15]
	s_mov_b32 m0, s57
	s_nop 0
	global_load_lds_dwordx4 v[82:83], off
	s_waitcnt vmcnt(8)
	s_waitcnt lgkmcnt(0)
	s_setprio 1
	s_barrier
	v_mfma_f32_16x16x32_bf16 v[82:85], v[50:53], v[66:69], v[94:97]
	v_mfma_f32_16x16x32_bf16 v[94:97], v[54:57], v[70:73], v[82:85]
	v_mfma_f32_16x16x32_bf16 v[82:85], v[58:61], v[66:69], v[90:93]
	v_mfma_f32_16x16x32_bf16 v[78:81], v[50:53], v[192:195], v[78:81]
	v_mfma_f32_16x16x32_bf16 v[74:77], v[58:61], v[192:195], v[74:77]
	v_mfma_f32_16x16x32_bf16 v[30:33], v[50:53], v[210:213], v[30:33]
	v_mfma_f32_16x16x32_bf16 v[26:29], v[58:61], v[210:213], v[26:29]
	v_mfma_f32_16x16x32_bf16 v[14:17], v[50:53], v[218:221], v[14:17]
	v_mfma_f32_16x16x32_bf16 v[10:13], v[58:61], v[218:221], v[10:13]
	v_mfma_f32_16x16x32_bf16 v[90:93], v[62:65], v[70:73], v[82:85]
	v_mfma_f32_16x16x32_bf16 v[78:81], v[54:57], v[196:199], v[78:81]
	v_mfma_f32_16x16x32_bf16 v[74:77], v[62:65], v[196:199], v[74:77]
	v_mfma_f32_16x16x32_bf16 v[30:33], v[54:57], v[214:217], v[30:33]
	v_mfma_f32_16x16x32_bf16 v[26:29], v[62:65], v[214:217], v[26:29]
	v_mfma_f32_16x16x32_bf16 v[14:17], v[54:57], v[222:225], v[14:17]
	v_mfma_f32_16x16x32_bf16 v[10:13], v[62:65], v[222:225], v[10:13]
	v_mfma_f32_16x16x32_bf16 v[34:37], v[172:175], v[66:69], v[34:37]
	v_mfma_f32_16x16x32_bf16 v[86:89], v[180:183], v[70:73], v[34:37]
	v_mfma_f32_16x16x32_bf16 v[34:37], v[184:187], v[66:69], v[38:41]
	v_mfma_f32_16x16x32_bf16 v[82:85], v[188:191], v[70:73], v[34:37]
	v_mfma_f32_16x16x32_bf16 v[34:37], v[172:175], v[192:195], v[42:45]
	v_mfma_f32_16x16x32_bf16 v[70:73], v[180:183], v[196:199], v[34:37]
	v_mfma_f32_16x16x32_bf16 v[34:37], v[184:187], v[192:195], v[46:49]
	v_mfma_f32_16x16x32_bf16 v[22:25], v[172:175], v[210:213], v[22:25]
	v_mfma_f32_16x16x32_bf16 v[18:21], v[184:187], v[210:213], v[18:21]
	v_mfma_f32_16x16x32_bf16 v[6:9], v[172:175], v[218:221], v[6:9]
	v_mfma_f32_16x16x32_bf16 v[2:5], v[184:187], v[218:221], v[2:5]
	v_mfma_f32_16x16x32_bf16 v[66:69], v[188:191], v[196:199], v[34:37]
	v_mfma_f32_16x16x32_bf16 v[22:25], v[180:183], v[214:217], v[22:25]
	v_mfma_f32_16x16x32_bf16 v[18:21], v[188:191], v[214:217], v[18:21]
	v_mfma_f32_16x16x32_bf16 v[6:9], v[180:183], v[222:225], v[6:9]
	v_mfma_f32_16x16x32_bf16 v[2:5], v[188:191], v[222:225], v[2:5]
	s_setprio 0
	s_barrier
	s_add_u32 s52, s52, 0x100
	s_addc_u32 s53, s53, 0
	s_add_u32 s67, s67, 0x100
	s_addc_u32 s68, s68, 0
	s_cmp_ge_i32 s69, s58
	s_mov_b32 s54, s69
	s_cbranch_scc0 .LBB0_1873

.LBB0_1953:
	s_add_i32 s44, s40, 2
	s_add_u32 s7, s38, 0x80
	s_addc_u32 s10, s39, 0
	s_add_i32 s45, 0, 0x10000
	s_cmp_eq_u32 s74, s40
	s_cselect_b32 s41, s65, s10
	s_cselect_b32 s40, s64, s7
	v_add_u32_e32 v0, s45, v247
	s_cselect_b32 s11, s67, s43
	s_cselect_b32 s10, s66, s42
	s_add_i32 s7, 0, 0x14000
	ds_read_b128 v[18:21], v0
	ds_read_b128 v[22:25], v0 offset:1024
	ds_read_b128 v[26:29], v0 offset:2048
	ds_read_b128 v[30:33], v0 offset:3072
	v_add_u32_e32 v0, s7, v247
	ds_read_b128 v[42:45], v0
	ds_read_b128 v[46:49], v0 offset:1024
	ds_read_b128 v[58:61], v0 offset:2048
	ds_read_b128 v[62:65], v0 offset:3072
	v_lshl_add_u64 v[202:203], s[38:39], 0, v[198:199]
	s_add_i32 m0, s17, 0xc000
	ds_read_b128 v[122:125], v248
	ds_read_b128 v[134:137], v248 offset:1024
	ds_read_b128 v[146:149], v248 offset:2048
	ds_read_b128 v[158:161], v248 offset:3072
	ds_read_b128 v[170:173], v248 offset:4096
	ds_read_b128 v[182:185], v248 offset:5120
	ds_read_b128 v[186:189], v248 offset:6144
	ds_read_b128 v[210:213], v248 offset:7168
	global_load_lds_dwordx4 v[202:203], off
	v_lshl_add_u64 v[202:203], s[38:39], 0, v[200:201]
	s_add_i32 m0, s17, 0xe000
	s_nop 0
	global_load_lds_dwordx4 v[202:203], off
	s_waitcnt vmcnt(8)
	s_waitcnt lgkmcnt(0)
	s_setprio 1
	s_barrier
	v_mfma_f32_16x16x32_bf16 v[174:177], v[18:21], v[122:125], v[174:177]
	v_mfma_f32_16x16x32_bf16 v[178:181], v[26:29], v[122:125], v[178:181]
	v_mfma_f32_16x16x32_bf16 v[154:157], v[18:21], v[146:149], v[154:157]
	v_mfma_f32_16x16x32_bf16 v[150:153], v[26:29], v[146:149], v[150:153]
	v_mfma_f32_16x16x32_bf16 v[130:133], v[18:21], v[170:173], v[130:133]
	v_mfma_f32_16x16x32_bf16 v[126:129], v[26:29], v[170:173], v[126:129]
	v_mfma_f32_16x16x32_bf16 v[110:113], v[18:21], v[186:189], v[110:113]
	v_mfma_f32_16x16x32_bf16 v[106:109], v[26:29], v[186:189], v[106:109]
	v_mfma_f32_16x16x32_bf16 v[174:177], v[22:25], v[134:137], v[174:177]
	v_mfma_f32_16x16x32_bf16 v[178:181], v[30:33], v[134:137], v[178:181]
	v_mfma_f32_16x16x32_bf16 v[154:157], v[22:25], v[158:161], v[154:157]
	v_mfma_f32_16x16x32_bf16 v[150:153], v[30:33], v[158:161], v[150:153]
	v_mfma_f32_16x16x32_bf16 v[130:133], v[22:25], v[182:185], v[130:133]
	v_mfma_f32_16x16x32_bf16 v[126:129], v[30:33], v[182:185], v[126:129]
	v_mfma_f32_16x16x32_bf16 v[110:113], v[22:25], v[210:213], v[110:113]
	v_mfma_f32_16x16x32_bf16 v[106:109], v[30:33], v[210:213], v[106:109]
	v_mfma_f32_16x16x32_bf16 v[166:169], v[42:45], v[122:125], v[166:169]
	v_mfma_f32_16x16x32_bf16 v[122:125], v[58:61], v[122:125], v[162:165]
	v_mfma_f32_16x16x32_bf16 v[138:141], v[58:61], v[146:149], v[138:141]
	v_mfma_f32_16x16x32_bf16 v[118:121], v[42:45], v[170:173], v[118:121]
	v_mfma_f32_16x16x32_bf16 v[114:117], v[58:61], v[170:173], v[114:117]
	v_mfma_f32_16x16x32_bf16 v[102:105], v[42:45], v[186:189], v[102:105]
	v_mfma_f32_16x16x32_bf16 v[98:101], v[58:61], v[186:189], v[98:101]
	v_mfma_f32_16x16x32_bf16 v[166:169], v[46:49], v[134:137], v[166:169]
	v_mfma_f32_16x16x32_bf16 v[122:125], v[62:65], v[134:137], v[122:125]
	v_mfma_f32_16x16x32_bf16 v[134:137], v[42:45], v[146:149], v[142:145]
	v_mfma_f32_16x16x32_bf16 v[138:141], v[62:65], v[158:161], v[138:141]
	v_mfma_f32_16x16x32_bf16 v[118:121], v[46:49], v[182:185], v[118:121]
	v_mfma_f32_16x16x32_bf16 v[114:117], v[62:65], v[182:185], v[114:117]
	v_mfma_f32_16x16x32_bf16 v[102:105], v[46:49], v[210:213], v[102:105]
	v_mfma_f32_16x16x32_bf16 v[98:101], v[62:65], v[210:213], v[98:101]
	v_mfma_f32_16x16x32_bf16 v[134:137], v[46:49], v[158:161], v[134:137]
	s_setprio 0
	s_barrier
	s_add_i32 s45, s45, s16
	v_lshl_add_u64 v[202:203], s[10:11], 0, v[192:193]
	s_mov_b32 m0, s45
	ds_read_b128 v[142:145], v248 offset:16384
	ds_read_b128 v[146:149], v248 offset:17408
	ds_read_b128 v[158:161], v248 offset:18432
	ds_read_b128 v[162:165], v248 offset:19456
	ds_read_b128 v[170:173], v248 offset:20480
	ds_read_b128 v[182:185], v248 offset:21504
	ds_read_b128 v[186:189], v248 offset:22528
	ds_read_b128 v[210:213], v248 offset:23552
	global_load_lds_dwordx4 v[202:203], off
	s_add_i32 m0, s45, 0x2000
	v_lshl_add_u64 v[222:223], s[10:11], 0, v[196:197]
	s_add_u32 s10, s10, s0
	s_addc_u32 s11, s11, s1
	s_add_i32 s7, s7, s16
	global_load_lds_dwordx4 v[222:223], off
	v_lshl_add_u64 v[224:225], s[10:11], 0, v[192:193]
	s_mov_b32 m0, s7
	v_lshl_add_u64 v[226:227], s[10:11], 0, v[196:197]
	global_load_lds_dwordx4 v[224:225], off
	s_add_i32 m0, s7, 0x2000
	v_lshl_add_u64 v[228:229], s[40:41], 0, v[190:191]
	global_load_lds_dwordx4 v[226:227], off
	s_mov_b32 m0, s17
	v_lshl_add_u64 v[230:231], s[40:41], 0, v[194:195]
	global_load_lds_dwordx4 v[228:229], off
	s_mov_b32 m0, s23
	s_nop 0
	global_load_lds_dwordx4 v[230:231], off
	s_waitcnt vmcnt(8)
	s_waitcnt lgkmcnt(0)
	s_setprio 1
	s_barrier
	v_mfma_f32_16x16x32_bf16 v[94:97], v[18:21], v[142:145], v[94:97]
	v_mfma_f32_16x16x32_bf16 v[90:93], v[26:29], v[142:145], v[90:93]
	v_mfma_f32_16x16x32_bf16 v[78:81], v[18:21], v[158:161], v[78:81]
	v_mfma_f32_16x16x32_bf16 v[74:77], v[26:29], v[158:161], v[74:77]
	v_mfma_f32_16x16x32_bf16 v[54:57], v[18:21], v[170:173], v[54:57]
	v_mfma_f32_16x16x32_bf16 v[50:53], v[26:29], v[170:173], v[50:53]
	v_mfma_f32_16x16x32_bf16 v[14:17], v[18:21], v[186:189], v[14:17]
	v_mfma_f32_16x16x32_bf16 v[10:13], v[26:29], v[186:189], v[10:13]
	v_mfma_f32_16x16x32_bf16 v[94:97], v[22:25], v[146:149], v[94:97]
	v_mfma_f32_16x16x32_bf16 v[90:93], v[30:33], v[146:149], v[90:93]
	v_mfma_f32_16x16x32_bf16 v[78:81], v[22:25], v[162:165], v[78:81]
	v_mfma_f32_16x16x32_bf16 v[74:77], v[30:33], v[162:165], v[74:77]
	v_mfma_f32_16x16x32_bf16 v[54:57], v[22:25], v[182:185], v[54:57]
	v_mfma_f32_16x16x32_bf16 v[50:53], v[30:33], v[182:185], v[50:53]
	v_mfma_f32_16x16x32_bf16 v[14:17], v[22:25], v[210:213], v[14:17]
	v_mfma_f32_16x16x32_bf16 v[10:13], v[30:33], v[210:213], v[10:13]
	v_mfma_f32_16x16x32_bf16 v[38:41], v[42:45], v[170:173], v[38:41]
	v_mfma_f32_16x16x32_bf16 v[34:37], v[58:61], v[170:173], v[34:37]
	v_mfma_f32_16x16x32_bf16 v[6:9], v[42:45], v[186:189], v[6:9]
	v_mfma_f32_16x16x32_bf16 v[2:5], v[58:61], v[186:189], v[2:5]
	v_mfma_f32_16x16x32_bf16 v[18:21], v[42:45], v[142:145], v[86:89]
	v_mfma_f32_16x16x32_bf16 v[22:25], v[58:61], v[142:145], v[82:85]
	v_mfma_f32_16x16x32_bf16 v[26:29], v[42:45], v[158:161], v[70:73]
	v_mfma_f32_16x16x32_bf16 v[30:33], v[58:61], v[158:161], v[66:69]
	v_mfma_f32_16x16x32_bf16 v[38:41], v[46:49], v[182:185], v[38:41]
	v_mfma_f32_16x16x32_bf16 v[34:37], v[62:65], v[182:185], v[34:37]
	v_mfma_f32_16x16x32_bf16 v[6:9], v[46:49], v[210:213], v[6:9]
	v_mfma_f32_16x16x32_bf16 v[2:5], v[62:65], v[210:213], v[2:5]
	v_mfma_f32_16x16x32_bf16 v[18:21], v[46:49], v[146:149], v[18:21]
	v_mfma_f32_16x16x32_bf16 v[22:25], v[62:65], v[146:149], v[22:25]
	v_mfma_f32_16x16x32_bf16 v[26:29], v[46:49], v[162:165], v[26:29]
	v_mfma_f32_16x16x32_bf16 v[30:33], v[62:65], v[162:165], v[30:33]
	s_setprio 0
	s_barrier
	s_add_i32 s7, 0, 0x18000
	v_add_u32_e32 v0, s7, v247
	s_add_i32 s45, 0, 0x1c000
	ds_read_b128 v[42:45], v0
	ds_read_b128 v[46:49], v0 offset:1024
	ds_read_b128 v[58:61], v0 offset:2048
	ds_read_b128 v[62:65], v0 offset:3072
	v_add_u32_e32 v0, s45, v247
	ds_read_b128 v[146:149], v0
	ds_read_b128 v[158:161], v0 offset:1024
	ds_read_b128 v[170:173], v0 offset:2048
	ds_read_b128 v[182:185], v0 offset:3072
	s_add_u32 s10, s40, s0
	s_addc_u32 s11, s41, s1
	s_mov_b32 m0, s68
	v_lshl_add_u64 v[142:143], s[10:11], 0, v[190:191]
	ds_read_b128 v[66:69], v248 offset:32768
	ds_read_b128 v[70:73], v248 offset:33792
	ds_read_b128 v[82:85], v248 offset:34816
	ds_read_b128 v[86:89], v248 offset:35840
	ds_read_b128 v[186:189], v248 offset:36864
	ds_read_b128 v[210:213], v248 offset:37888
	ds_read_b128 v[214:217], v248 offset:38912
	ds_read_b128 v[218:221], v248 offset:39936
	global_load_lds_dwordx4 v[142:143], off
	v_lshl_add_u64 v[142:143], s[10:11], 0, v[194:195]
	s_mov_b32 m0, s69
	s_nop 0
	global_load_lds_dwordx4 v[142:143], off
	s_waitcnt vmcnt(8)
	s_waitcnt lgkmcnt(0)
	s_setprio 1
	s_barrier
	v_mfma_f32_16x16x32_bf16 v[142:145], v[42:45], v[66:69], v[174:177]
	v_mfma_f32_16x16x32_bf16 v[174:177], v[46:49], v[70:73], v[142:145]
	v_mfma_f32_16x16x32_bf16 v[142:145], v[58:61], v[66:69], v[178:181]
	v_mfma_f32_16x16x32_bf16 v[178:181], v[62:65], v[70:73], v[142:145]
	v_mfma_f32_16x16x32_bf16 v[142:145], v[42:45], v[82:85], v[154:157]
	v_mfma_f32_16x16x32_bf16 v[154:157], v[46:49], v[86:89], v[142:145]
	v_mfma_f32_16x16x32_bf16 v[142:145], v[58:61], v[82:85], v[150:153]
	v_mfma_f32_16x16x32_bf16 v[130:133], v[42:45], v[186:189], v[130:133]
	v_mfma_f32_16x16x32_bf16 v[126:129], v[58:61], v[186:189], v[126:129]
	v_mfma_f32_16x16x32_bf16 v[110:113], v[42:45], v[214:217], v[110:113]
	v_mfma_f32_16x16x32_bf16 v[106:109], v[58:61], v[214:217], v[106:109]
	v_mfma_f32_16x16x32_bf16 v[150:153], v[62:65], v[86:89], v[142:145]
	v_mfma_f32_16x16x32_bf16 v[130:133], v[46:49], v[210:213], v[130:133]
	v_mfma_f32_16x16x32_bf16 v[126:129], v[62:65], v[210:213], v[126:129]
	v_mfma_f32_16x16x32_bf16 v[110:113], v[46:49], v[218:221], v[110:113]
	v_mfma_f32_16x16x32_bf16 v[106:109], v[62:65], v[218:221], v[106:109]
	v_mfma_f32_16x16x32_bf16 v[142:145], v[146:149], v[66:69], v[166:169]
	v_mfma_f32_16x16x32_bf16 v[66:69], v[170:173], v[66:69], v[122:125]
	v_mfma_f32_16x16x32_bf16 v[162:165], v[182:185], v[70:73], v[66:69]
	v_mfma_f32_16x16x32_bf16 v[66:69], v[146:149], v[82:85], v[134:137]
	v_mfma_f32_16x16x32_bf16 v[166:169], v[158:161], v[70:73], v[142:145]
	v_mfma_f32_16x16x32_bf16 v[142:145], v[158:161], v[86:89], v[66:69]
	v_mfma_f32_16x16x32_bf16 v[66:69], v[170:173], v[82:85], v[138:141]
	v_mfma_f32_16x16x32_bf16 v[138:141], v[182:185], v[86:89], v[66:69]
	v_mfma_f32_16x16x32_bf16 v[66:69], v[146:149], v[186:189], v[118:121]
	v_mfma_f32_16x16x32_bf16 v[118:121], v[158:161], v[210:213], v[66:69]
	v_mfma_f32_16x16x32_bf16 v[66:69], v[170:173], v[186:189], v[114:117]
	v_mfma_f32_16x16x32_bf16 v[114:117], v[182:185], v[210:213], v[66:69]
	v_mfma_f32_16x16x32_bf16 v[66:69], v[146:149], v[214:217], v[102:105]
	v_mfma_f32_16x16x32_bf16 v[102:105], v[158:161], v[218:221], v[66:69]
	v_mfma_f32_16x16x32_bf16 v[66:69], v[170:173], v[214:217], v[98:101]
	v_mfma_f32_16x16x32_bf16 v[98:101], v[182:185], v[218:221], v[66:69]
	s_setprio 0
	s_barrier
	s_add_i32 s7, s7, s16
	v_lshl_add_u64 v[82:83], v[202:203], 0, s[14:15]
	s_mov_b32 m0, s7
	s_nop 1
	ds_read_b128 v[66:69], v248 offset:49152
	ds_read_b128 v[70:73], v248 offset:50176
	ds_read_b128 v[122:125], v248 offset:51200
	ds_read_b128 v[134:137], v248 offset:52224
	ds_read_b128 v[186:189], v248 offset:53248
	ds_read_b128 v[210:213], v248 offset:54272
	ds_read_b128 v[214:217], v248 offset:55296
	ds_read_b128 v[218:221], v248 offset:56320
	global_load_lds_dwordx4 v[82:83], off
	v_lshl_add_u64 v[82:83], v[222:223], 0, s[14:15]
	s_add_i32 m0, s7, 0x2000
	s_add_i32 s7, s45, s16
	global_load_lds_dwordx4 v[82:83], off
	v_lshl_add_u64 v[82:83], v[224:225], 0, s[14:15]
	s_mov_b32 m0, s7
	s_nop 0
	global_load_lds_dwordx4 v[82:83], off
	v_lshl_add_u64 v[82:83], v[226:227], 0, s[14:15]
	s_add_i32 m0, s7, 0x2000
	s_nop 0
	global_load_lds_dwordx4 v[82:83], off
	v_lshl_add_u64 v[82:83], v[228:229], 0, s[14:15]
	s_mov_b32 m0, s8
	s_nop 0
	global_load_lds_dwordx4 v[82:83], off
	v_lshl_add_u64 v[82:83], v[230:231], 0, s[14:15]
	s_mov_b32 m0, s70
	s_nop 0
	global_load_lds_dwordx4 v[82:83], off
	s_waitcnt vmcnt(8)
	s_waitcnt lgkmcnt(0)
	s_setprio 1
	s_barrier
	v_mfma_f32_16x16x32_bf16 v[82:85], v[42:45], v[66:69], v[94:97]
	v_mfma_f32_16x16x32_bf16 v[94:97], v[46:49], v[70:73], v[82:85]
	v_mfma_f32_16x16x32_bf16 v[82:85], v[58:61], v[66:69], v[90:93]
	v_mfma_f32_16x16x32_bf16 v[78:81], v[42:45], v[122:125], v[78:81]
	v_mfma_f32_16x16x32_bf16 v[74:77], v[58:61], v[122:125], v[74:77]
	v_mfma_f32_16x16x32_bf16 v[54:57], v[42:45], v[186:189], v[54:57]
	v_mfma_f32_16x16x32_bf16 v[50:53], v[58:61], v[186:189], v[50:53]
	v_mfma_f32_16x16x32_bf16 v[14:17], v[42:45], v[214:217], v[14:17]
	v_mfma_f32_16x16x32_bf16 v[10:13], v[58:61], v[214:217], v[10:13]
	v_mfma_f32_16x16x32_bf16 v[90:93], v[62:65], v[70:73], v[82:85]
	v_mfma_f32_16x16x32_bf16 v[78:81], v[46:49], v[134:137], v[78:81]
	v_mfma_f32_16x16x32_bf16 v[74:77], v[62:65], v[134:137], v[74:77]
	v_mfma_f32_16x16x32_bf16 v[54:57], v[46:49], v[210:213], v[54:57]
	v_mfma_f32_16x16x32_bf16 v[50:53], v[62:65], v[210:213], v[50:53]
	v_mfma_f32_16x16x32_bf16 v[14:17], v[46:49], v[218:221], v[14:17]
	v_mfma_f32_16x16x32_bf16 v[10:13], v[62:65], v[218:221], v[10:13]
	v_mfma_f32_16x16x32_bf16 v[18:21], v[146:149], v[66:69], v[18:21]
	v_mfma_f32_16x16x32_bf16 v[86:89], v[158:161], v[70:73], v[18:21]
	v_mfma_f32_16x16x32_bf16 v[18:21], v[170:173], v[66:69], v[22:25]
	v_mfma_f32_16x16x32_bf16 v[82:85], v[182:185], v[70:73], v[18:21]
	v_mfma_f32_16x16x32_bf16 v[18:21], v[146:149], v[122:125], v[26:29]
	v_mfma_f32_16x16x32_bf16 v[70:73], v[158:161], v[134:137], v[18:21]
	v_mfma_f32_16x16x32_bf16 v[18:21], v[170:173], v[122:125], v[30:33]
	v_mfma_f32_16x16x32_bf16 v[66:69], v[182:185], v[134:137], v[18:21]
	v_mfma_f32_16x16x32_bf16 v[18:21], v[146:149], v[186:189], v[38:41]
	v_mfma_f32_16x16x32_bf16 v[38:41], v[158:161], v[210:213], v[18:21]
	v_mfma_f32_16x16x32_bf16 v[18:21], v[170:173], v[186:189], v[34:37]
	v_mfma_f32_16x16x32_bf16 v[6:9], v[146:149], v[214:217], v[6:9]
	v_mfma_f32_16x16x32_bf16 v[2:5], v[170:173], v[214:217], v[2:5]
	v_mfma_f32_16x16x32_bf16 v[34:37], v[182:185], v[210:213], v[18:21]
	v_mfma_f32_16x16x32_bf16 v[6:9], v[158:161], v[218:221], v[6:9]
	v_mfma_f32_16x16x32_bf16 v[2:5], v[182:185], v[218:221], v[2:5]
	s_setprio 0
	s_barrier
	s_add_u32 s38, s38, 0x100
	s_addc_u32 s39, s39, 0
	s_add_u32 s42, s42, 0x100
	s_addc_u32 s43, s43, 0
	s_cmp_ge_i32 s44, s71
	s_mov_b32 s40, s44
	s_cbranch_scc0 .LBB0_1953
